# K-loop MFMA segments start with the first MFMA right after the barrier (redundant lgkmcnt(0) removed, 28 sites), on top of the single early priority raise
# baseline (speedup 1.0000x reference)
; #define PG8_STAGE(bufoff, gbase, voff) do { _Pragma("unroll") for (int _i = 0; _i < 2; ++_i) \
;         __builtin_amdgcn_global_load_lds((const unsigned*)((const char*)(gbase) + (voff)[_i]), (PG8_LAS unsigned*)(lds + (bufoff) + ldsw + _i * 8192), 16, 0, 0); } while (0)
; #define PG8_LDA(dst, b, h) do { _Pragma("unroll") for (int m = 0; m < 4; ++m) { const bf16x8 f0_ = *(const PG8_LAS bf16x8*)(lds + PG8_SA(b, h) + aoff + m * 2048), f1_ = *(const PG8_LAS bf16x8*)(lds + PG8_SA(b, h) + aoff + m * 2048 + 1024); dst[m].set(f0_, f1_); } } while (0)
; #define PG8_LDB(dst, b, h) do { _Pragma("unroll") for (int n = 0; n < 2; ++n) { const bf16x8 f0_ = *(const PG8_LAS bf16x8*)(lds + PG8_SB(b, h) + boff + n * 2048), f1_ = *(const PG8_LAS bf16x8*)(lds + PG8_SB(b, h) + boff + n * 2048 + 1024); dst[n].set(f0_, f1_); } } while (0)
; #define PG8_WAIT_V(n) asm volatile("s_waitcnt vmcnt(" #n ")" ::: "memory")
; #define PG8_WAIT_L(n) asm volatile("s_waitcnt lgkmcnt(" #n ")" ::: "memory")
; #define PG8_BAR __builtin_amdgcn_s_barrier()
; #define PG8_SCHED __builtin_amdgcn_sched_barrier(0)
; template <class Epi, class Sched, bool ALIGN_EPI = false, bool SP2 = false>
; __device__ __forceinline__ void gemm_phase(PG8_LAS unsigned char* lds, const Gemm g, const Sched& S, const Epi& E) {
;     ...
;             PG8_LDB(B0, 0, 0); PG8_LDB(B1, 0, 1); PG8_SCHED; PG8_LDA(At, 0, 0); PG8_STAGE(PG8_SA(1, 1), a1 + hstep, voffA);
;             PG8_WAIT_V(8); PG8_WAIT_L(0); PG8_BAR; PG8_MMA(0, 0, At, B0); PG8_MMA(0, 1, At, B1); PG8_BAR; PG8_SCHED;
;             PG8_LDA(At, 0, 1); PG8_STAGE(PG8_SB(0, 0), b2, voffB); PG8_STAGE(PG8_SB(0, 1), b2 + hstepB, voffB); PG8_STAGE(PG8_SA(0, 0), a2, voffA);
;             PG8_WAIT_V(8); PG8_WAIT_L(0); PG8_BAR; PG8_MMA(1, 0, At, B0); PG8_MMA(1, 1, At, B1); PG8_BAR; PG8_SCHED;
.Lkr0_a:
	v_lshl_add_u64 v[190:191], s[2:3], 0, v[174:175]
	s_add_i32 m0, s58, 0xc000
	ds_read_b128 v[182:185], v205
	ds_read_b128 v[186:189], v205 offset:1024
	ds_read_b128 v[212:215], v205 offset:2048
	ds_read_b128 v[216:219], v205 offset:3072
	ds_read_b128 v[220:223], v205 offset:4096
	ds_read_b128 v[224:227], v205 offset:5120
	ds_read_b128 v[228:231], v205 offset:6144
	ds_read_b128 v[232:235], v205 offset:7168
	global_load_lds_dwordx4 v[190:191], off
	v_lshl_add_u64 v[190:191], s[2:3], 0, v[176:177]
	s_add_i32 m0, s58, 0xe000
	s_nop 0
	global_load_lds_dwordx4 v[190:191], off
	s_waitcnt vmcnt(8)
	s_waitcnt lgkmcnt(0)
	s_setprio 1
	s_barrier
	v_mfma_scale_f32_16x16x128_f8f6f4 v[158:161], v[18:25], v[182:189], v[158:161], v206, v207 op_sel_hi:[0,0,0]
	v_mfma_scale_f32_16x16x128_f8f6f4 v[154:157], v[26:33], v[182:189], v[154:157], v206, v207 op_sel_hi:[0,0,0]
	v_mfma_scale_f32_16x16x128_f8f6f4 v[142:145], v[18:25], v[212:219], v[142:145], v206, v207 op_sel_hi:[0,0,0]
	v_mfma_scale_f32_16x16x128_f8f6f4 v[138:141], v[26:33], v[212:219], v[138:141], v206, v207 op_sel_hi:[0,0,0]
	v_mfma_scale_f32_16x16x128_f8f6f4 v[126:129], v[18:25], v[220:227], v[126:129], v206, v207 op_sel_hi:[0,0,0]
	v_mfma_scale_f32_16x16x128_f8f6f4 v[122:125], v[26:33], v[220:227], v[122:125], v206, v207 op_sel_hi:[0,0,0]
	v_mfma_scale_f32_16x16x128_f8f6f4 v[110:113], v[18:25], v[228:235], v[110:113], v206, v207 op_sel_hi:[0,0,0]
	v_mfma_scale_f32_16x16x128_f8f6f4 v[106:109], v[26:33], v[228:235], v[106:109], v206, v207 op_sel_hi:[0,0,0]
	v_mfma_scale_f32_16x16x128_f8f6f4 v[150:153], v[2:9], v[182:189], v[150:153], v206, v207 op_sel_hi:[0,0,0]
	v_mfma_scale_f32_16x16x128_f8f6f4 v[146:149], v[10:17], v[182:189], v[146:149], v206, v207 op_sel_hi:[0,0,0]
	v_mfma_scale_f32_16x16x128_f8f6f4 v[134:137], v[2:9], v[212:219], v[134:137], v206, v207 op_sel_hi:[0,0,0]
	v_mfma_scale_f32_16x16x128_f8f6f4 v[130:133], v[10:17], v[212:219], v[130:133], v206, v207 op_sel_hi:[0,0,0]
	v_mfma_scale_f32_16x16x128_f8f6f4 v[118:121], v[2:9], v[220:227], v[118:121], v206, v207 op_sel_hi:[0,0,0]
	v_mfma_scale_f32_16x16x128_f8f6f4 v[114:117], v[10:17], v[220:227], v[114:117], v206, v207 op_sel_hi:[0,0,0]
	v_mfma_scale_f32_16x16x128_f8f6f4 v[102:105], v[2:9], v[228:235], v[102:105], v206, v207 op_sel_hi:[0,0,0]
	v_mfma_scale_f32_16x16x128_f8f6f4 v[98:101], v[10:17], v[228:235], v[98:101], v206, v207 op_sel_hi:[0,0,0]
	s_setprio 0
	s_barrier
	s_add_i32 s0, s76, s57
	v_lshl_add_u64 v[182:183], s[50:51], 0, v[164:165]
	s_mov_b32 m0, s0
	ds_read_b128 v[212:215], v205 offset:16384
	ds_read_b128 v[216:219], v205 offset:17408
	ds_read_b128 v[220:223], v205 offset:18432
	ds_read_b128 v[224:227], v205 offset:19456
	ds_read_b128 v[228:231], v205 offset:20480
	ds_read_b128 v[232:235], v205 offset:21504
	ds_read_b128 v[236:239], v205 offset:22528
	ds_read_b128 v[240:243], v205 offset:23552
	global_load_lds_dwordx4 v[182:183], off
	s_add_i32 m0, s0, 0x2000
	v_lshl_add_u64 v[184:185], s[50:51], 0, v[168:169]
	s_add_u32 s50, s50, s16
	s_addc_u32 s51, s51, s17
	s_add_i32 s0, s77, s57
	global_load_lds_dwordx4 v[184:185], off
	v_lshl_add_u64 v[186:187], s[50:51], 0, v[164:165]
	s_mov_b32 m0, s0
	v_lshl_add_u64 v[188:189], s[50:51], 0, v[168:169]
	global_load_lds_dwordx4 v[186:187], off
	s_add_i32 m0, s0, 0x2000
	v_lshl_add_u64 v[190:191], s[48:49], 0, v[162:163]
	global_load_lds_dwordx4 v[188:189], off
	v_lshl_add_u64 v[192:193], s[48:49], 0, v[166:167]
	s_waitcnt vmcnt(6)
	s_waitcnt lgkmcnt(0)
	s_setprio 1
	s_barrier
	v_mfma_scale_f32_16x16x128_f8f6f4 v[94:97], v[18:25], v[212:219], v[94:97], v206, v207 op_sel_hi:[0,0,0]
	v_mfma_scale_f32_16x16x128_f8f6f4 v[90:93], v[26:33], v[212:219], v[90:93], v206, v207 op_sel_hi:[0,0,0]
	v_mfma_scale_f32_16x16x128_f8f6f4 v[78:81], v[18:25], v[220:227], v[78:81], v206, v207 op_sel_hi:[0,0,0]
	v_mfma_scale_f32_16x16x128_f8f6f4 v[74:77], v[26:33], v[220:227], v[74:77], v206, v207 op_sel_hi:[0,0,0]
	v_mfma_scale_f32_16x16x128_f8f6f4 v[62:65], v[18:25], v[228:235], v[62:65], v206, v207 op_sel_hi:[0,0,0]
	v_mfma_scale_f32_16x16x128_f8f6f4 v[58:61], v[26:33], v[228:235], v[58:61], v206, v207 op_sel_hi:[0,0,0]
	v_mfma_scale_f32_16x16x128_f8f6f4 v[46:49], v[18:25], v[236:243], v[46:49], v206, v207 op_sel_hi:[0,0,0]
	v_mfma_scale_f32_16x16x128_f8f6f4 v[42:45], v[26:33], v[236:243], v[42:45], v206, v207 op_sel_hi:[0,0,0]
	v_mfma_scale_f32_16x16x128_f8f6f4 v[86:89], v[2:9], v[212:219], v[86:89], v206, v207 op_sel_hi:[0,0,0]
	v_mfma_scale_f32_16x16x128_f8f6f4 v[82:85], v[10:17], v[212:219], v[82:85], v206, v207 op_sel_hi:[0,0,0]
	v_mfma_scale_f32_16x16x128_f8f6f4 v[70:73], v[2:9], v[220:227], v[70:73], v206, v207 op_sel_hi:[0,0,0]
	v_mfma_scale_f32_16x16x128_f8f6f4 v[66:69], v[10:17], v[220:227], v[66:69], v206, v207 op_sel_hi:[0,0,0]
	v_mfma_scale_f32_16x16x128_f8f6f4 v[54:57], v[2:9], v[228:235], v[54:57], v206, v207 op_sel_hi:[0,0,0]
	v_mfma_scale_f32_16x16x128_f8f6f4 v[50:53], v[10:17], v[228:235], v[50:53], v206, v207 op_sel_hi:[0,0,0]
	v_mfma_scale_f32_16x16x128_f8f6f4 v[38:41], v[2:9], v[236:243], v[38:41], v206, v207 op_sel_hi:[0,0,0]
	v_mfma_scale_f32_16x16x128_f8f6f4 v[34:37], v[10:17], v[236:243], v[34:37], v206, v207 op_sel_hi:[0,0,0]
	s_setprio 0
	s_barrier
; #define PG8_STAGE(bufoff, gbase, voff) do { _Pragma("unroll") for (int _i = 0; _i < 2; ++_i) \
;         __builtin_amdgcn_global_load_lds((const unsigned*)((const char*)(gbase) + (voff)[_i]), (PG8_LAS unsigned*)(lds + (bufoff) + ldsw + _i * 8192), 16, 0, 0); } while (0)
; #define PG8_LDA(dst, b, h) do { _Pragma("unroll") for (int m = 0; m < 4; ++m) { const bf16x8 f0_ = *(const PG8_LAS bf16x8*)(lds + PG8_SA(b, h) + aoff + m * 2048), f1_ = *(const PG8_LAS bf16x8*)(lds + PG8_SA(b, h) + aoff + m * 2048 + 1024); dst[m].set(f0_, f1_); } } while (0)
; #define PG8_LDB(dst, b, h) do { _Pragma("unroll") for (int n = 0; n < 2; ++n) { const bf16x8 f0_ = *(const PG8_LAS bf16x8*)(lds + PG8_SB(b, h) + boff + n * 2048), f1_ = *(const PG8_LAS bf16x8*)(lds + PG8_SB(b, h) + boff + n * 2048 + 1024); dst[n].set(f0_, f1_); } } while (0)
; #define PG8_WAIT_V(n) asm volatile("s_waitcnt vmcnt(" #n ")" ::: "memory")
; #define PG8_WAIT_L(n) asm volatile("s_waitcnt lgkmcnt(" #n ")" ::: "memory")
; #define PG8_BAR __builtin_amdgcn_s_barrier()
; #define PG8_SCHED __builtin_amdgcn_sched_barrier(0)
; template <class Epi, class Sched, bool ALIGN_EPI = false, bool SP2 = false>
; __device__ __forceinline__ void gemm_phase(PG8_LAS unsigned char* lds, const Gemm g, const Sched& S, const Epi& E) {
;     ...
;             PG8_LDB(B0, 1, 0); PG8_LDB(B1, 1, 1); PG8_SCHED; PG8_LDA(At, 1, 0); PG8_STAGE(PG8_SA(0, 1), a2 + hstep, voffA);
;             PG8_WAIT_V(8); PG8_WAIT_L(0); PG8_BAR; PG8_MMA(0, 0, At, B0); PG8_MMA(0, 1, At, B1); PG8_BAR; PG8_SCHED;
;             PG8_LDA(At, 1, 1); PG8_STAGE(PG8_SB(1, 0), b3, voffB); PG8_STAGE(PG8_SB(1, 1), b3 + hstepB, voffB); PG8_STAGE(PG8_SA(1, 0), a3, voffA);
;             PG8_WAIT_V(8); PG8_WAIT_L(0); PG8_BAR; PG8_MMA(1, 0, At, B0); PG8_MMA(1, 1, At, B1); PG8_BAR; PG8_SCHED;
	s_add_i32 s0, 0, 0x18000
	s_add_i32 s1, 0, 0x1c000
	v_add_u32_e32 v14, s0, v194
	v_add_u32_e32 v30, s1, v194
	ds_read_b128 v[2:5], v14
	ds_read_b128 v[6:9], v14 offset:1024
	ds_read_b128 v[10:13], v14 offset:2048
	ds_read_b128 v[14:17], v14 offset:3072
	ds_read_b128 v[18:21], v30
	ds_read_b128 v[22:25], v30 offset:1024
	ds_read_b128 v[26:29], v30 offset:2048
	ds_read_b128 v[30:33], v30 offset:3072
	s_add_u32 s48, s48, s14
	s_addc_u32 s49, s49, s15
	s_mov_b32 m0, s61
	v_lshl_add_u64 v[244:245], s[48:49], 0, v[162:163]
	ds_read_b128 v[212:215], v205 offset:32768
	ds_read_b128 v[216:219], v205 offset:33792
	ds_read_b128 v[220:223], v205 offset:34816
	ds_read_b128 v[224:227], v205 offset:35840
	ds_read_b128 v[228:231], v205 offset:36864
	ds_read_b128 v[232:235], v205 offset:37888
	ds_read_b128 v[236:239], v205 offset:38912
	ds_read_b128 v[240:243], v205 offset:39936
	s_mov_b32 m0, s58
	s_nop 0
	global_load_lds_dwordx4 v[190:191], off
	s_mov_b32 m0, s59
	s_nop 0
	global_load_lds_dwordx4 v[192:193], off
	s_mov_b32 m0, s61
	s_nop 0
	global_load_lds_dwordx4 v[244:245], off
	v_lshl_add_u64 v[244:245], s[48:49], 0, v[166:167]
	s_mov_b32 m0, s63
	s_nop 0
	global_load_lds_dwordx4 v[244:245], off
	s_waitcnt vmcnt(8)
	s_waitcnt lgkmcnt(0)
	s_setprio 1
	s_barrier
	v_mfma_scale_f32_16x16x128_f8f6f4 v[158:161], v[2:9], v[212:219], v[158:161], v206, v207 op_sel_hi:[0,0,0]
	v_mfma_scale_f32_16x16x128_f8f6f4 v[154:157], v[10:17], v[212:219], v[154:157], v206, v207 op_sel_hi:[0,0,0]
	v_mfma_scale_f32_16x16x128_f8f6f4 v[142:145], v[2:9], v[220:227], v[142:145], v206, v207 op_sel_hi:[0,0,0]
	v_mfma_scale_f32_16x16x128_f8f6f4 v[138:141], v[10:17], v[220:227], v[138:141], v206, v207 op_sel_hi:[0,0,0]
	v_mfma_scale_f32_16x16x128_f8f6f4 v[126:129], v[2:9], v[228:235], v[126:129], v206, v207 op_sel_hi:[0,0,0]
	v_mfma_scale_f32_16x16x128_f8f6f4 v[122:125], v[10:17], v[228:235], v[122:125], v206, v207 op_sel_hi:[0,0,0]
	v_mfma_scale_f32_16x16x128_f8f6f4 v[110:113], v[2:9], v[236:243], v[110:113], v206, v207 op_sel_hi:[0,0,0]
	v_mfma_scale_f32_16x16x128_f8f6f4 v[106:109], v[10:17], v[236:243], v[106:109], v206, v207 op_sel_hi:[0,0,0]
	v_mfma_scale_f32_16x16x128_f8f6f4 v[150:153], v[18:25], v[212:219], v[150:153], v206, v207 op_sel_hi:[0,0,0]
	v_mfma_scale_f32_16x16x128_f8f6f4 v[146:149], v[26:33], v[212:219], v[146:149], v206, v207 op_sel_hi:[0,0,0]
	v_mfma_scale_f32_16x16x128_f8f6f4 v[134:137], v[18:25], v[220:227], v[134:137], v206, v207 op_sel_hi:[0,0,0]
	v_mfma_scale_f32_16x16x128_f8f6f4 v[130:133], v[26:33], v[220:227], v[130:133], v206, v207 op_sel_hi:[0,0,0]
	v_mfma_scale_f32_16x16x128_f8f6f4 v[118:121], v[18:25], v[228:235], v[118:121], v206, v207 op_sel_hi:[0,0,0]
	v_mfma_scale_f32_16x16x128_f8f6f4 v[114:117], v[26:33], v[228:235], v[114:117], v206, v207 op_sel_hi:[0,0,0]
	v_mfma_scale_f32_16x16x128_f8f6f4 v[102:105], v[18:25], v[236:243], v[102:105], v206, v207 op_sel_hi:[0,0,0]
	v_mfma_scale_f32_16x16x128_f8f6f4 v[98:101], v[26:33], v[236:243], v[98:101], v206, v207 op_sel_hi:[0,0,0]
	s_setprio 0
	s_barrier
	s_add_i32 s0, s0, s57
	v_lshl_add_u64 v[182:183], v[182:183], 0, s[36:37]
	s_mov_b32 m0, s0
	ds_read_b128 v[212:215], v205 offset:49152
	ds_read_b128 v[216:219], v205 offset:50176
	ds_read_b128 v[220:223], v205 offset:51200
	ds_read_b128 v[224:227], v205 offset:52224
	ds_read_b128 v[228:231], v205 offset:53248
	ds_read_b128 v[232:235], v205 offset:54272
	ds_read_b128 v[236:239], v205 offset:55296
	ds_read_b128 v[240:243], v205 offset:56320
	global_load_lds_dwordx4 v[182:183], off
	v_lshl_add_u64 v[182:183], v[184:185], 0, s[36:37]
	s_add_i32 m0, s0, 0x2000
	s_add_i32 s0, s1, s57
	global_load_lds_dwordx4 v[182:183], off
	v_lshl_add_u64 v[182:183], v[186:187], 0, s[36:37]
	s_mov_b32 m0, s0
	s_nop 0
	global_load_lds_dwordx4 v[182:183], off
	v_lshl_add_u64 v[182:183], v[188:189], 0, s[36:37]
	s_add_i32 m0, s0, 0x2000
	s_nop 0
	global_load_lds_dwordx4 v[182:183], off
	s_cmp_ge_i32 s53, s69
	s_cbranch_scc0 .Lkr0_b
	v_lshl_add_u64 v[182:183], v[190:191], 0, s[36:37]
	s_mov_b32 m0, s66
	s_nop 0
	global_load_lds_dwordx4 v[182:183], off
	v_lshl_add_u64 v[182:183], v[192:193], 0, s[36:37]
	s_mov_b32 m0, s67
	s_nop 0
	global_load_lds_dwordx4 v[182:183], off
.Lkr0_b:
	s_waitcnt vmcnt(6)
	s_waitcnt lgkmcnt(0)
	s_setprio 1
	s_barrier
	v_mfma_scale_f32_16x16x128_f8f6f4 v[94:97], v[2:9], v[212:219], v[94:97], v206, v207 op_sel_hi:[0,0,0]
	v_mfma_scale_f32_16x16x128_f8f6f4 v[90:93], v[10:17], v[212:219], v[90:93], v206, v207 op_sel_hi:[0,0,0]
	v_mfma_scale_f32_16x16x128_f8f6f4 v[78:81], v[2:9], v[220:227], v[78:81], v206, v207 op_sel_hi:[0,0,0]
	v_mfma_scale_f32_16x16x128_f8f6f4 v[74:77], v[10:17], v[220:227], v[74:77], v206, v207 op_sel_hi:[0,0,0]
	v_mfma_scale_f32_16x16x128_f8f6f4 v[62:65], v[2:9], v[228:235], v[62:65], v206, v207 op_sel_hi:[0,0,0]
	v_mfma_scale_f32_16x16x128_f8f6f4 v[58:61], v[10:17], v[228:235], v[58:61], v206, v207 op_sel_hi:[0,0,0]
	v_mfma_scale_f32_16x16x128_f8f6f4 v[46:49], v[2:9], v[236:243], v[46:49], v206, v207 op_sel_hi:[0,0,0]
	v_mfma_scale_f32_16x16x128_f8f6f4 v[42:45], v[10:17], v[236:243], v[42:45], v206, v207 op_sel_hi:[0,0,0]
	v_mfma_scale_f32_16x16x128_f8f6f4 v[86:89], v[18:25], v[212:219], v[86:89], v206, v207 op_sel_hi:[0,0,0]
	v_mfma_scale_f32_16x16x128_f8f6f4 v[82:85], v[26:33], v[212:219], v[82:85], v206, v207 op_sel_hi:[0,0,0]
	v_mfma_scale_f32_16x16x128_f8f6f4 v[70:73], v[18:25], v[220:227], v[70:73], v206, v207 op_sel_hi:[0,0,0]
	v_mfma_scale_f32_16x16x128_f8f6f4 v[66:69], v[26:33], v[220:227], v[66:69], v206, v207 op_sel_hi:[0,0,0]
	v_mfma_scale_f32_16x16x128_f8f6f4 v[54:57], v[18:25], v[228:235], v[54:57], v206, v207 op_sel_hi:[0,0,0]
	v_mfma_scale_f32_16x16x128_f8f6f4 v[50:53], v[26:33], v[228:235], v[50:53], v206, v207 op_sel_hi:[0,0,0]
	v_mfma_scale_f32_16x16x128_f8f6f4 v[38:41], v[18:25], v[236:243], v[38:41], v206, v207 op_sel_hi:[0,0,0]
	v_mfma_scale_f32_16x16x128_f8f6f4 v[34:37], v[26:33], v[236:243], v[34:37], v206, v207 op_sel_hi:[0,0,0]
	s_setprio 0
	s_barrier
	s_add_u32 s2, s2, 0x100
	s_addc_u32 s3, s3, 0
	s_add_u32 s20, s20, 0x100
	s_addc_u32 s52, s52, 0
	s_cmp_ge_i32 s53, s69
	s_cselect_b32 s99, 0, 1
	s_mov_b32 s48, s53
	s_cbranch_scc0 .LBB0_204

; #define PG8_STAGE(bufoff, gbase, voff) do { _Pragma("unroll") for (int _i = 0; _i < 2; ++_i) \
;         __builtin_amdgcn_global_load_lds((const unsigned*)((const char*)(gbase) + (voff)[_i]), (PG8_LAS unsigned*)(lds + (bufoff) + ldsw + _i * 8192), 16, 0, 0); } while (0)
; #define PG8_LDA(dst, b, h) do { _Pragma("unroll") for (int m = 0; m < 4; ++m) { const bf16x8 f0_ = *(const PG8_LAS bf16x8*)(lds + PG8_SA(b, h) + aoff + m * 2048), f1_ = *(const PG8_LAS bf16x8*)(lds + PG8_SA(b, h) + aoff + m * 2048 + 1024); dst[m].set(f0_, f1_); } } while (0)
; #define PG8_LDB(dst, b, h) do { _Pragma("unroll") for (int n = 0; n < 2; ++n) { const bf16x8 f0_ = *(const PG8_LAS bf16x8*)(lds + PG8_SB(b, h) + boff + n * 2048), f1_ = *(const PG8_LAS bf16x8*)(lds + PG8_SB(b, h) + boff + n * 2048 + 1024); dst[n].set(f0_, f1_); } } while (0)
; #define PG8_WAIT_V(n) asm volatile("s_waitcnt vmcnt(" #n ")" ::: "memory")
; #define PG8_WAIT_L(n) asm volatile("s_waitcnt lgkmcnt(" #n ")" ::: "memory")
; #define PG8_BAR __builtin_amdgcn_s_barrier()
; #define PG8_SCHED __builtin_amdgcn_sched_barrier(0)
; template <class Epi, class Sched, bool ALIGN_EPI = false, bool SP2 = false>
; __device__ __forceinline__ void gemm_phase(PG8_LAS unsigned char* lds, const Gemm g, const Sched& S, const Epi& E) {
;     ...
;             const bool last = (t == nt - 2);
;             const char* a1 = cA + (size_t)(t + 1) * kstep;
;             const char* a2 = last ? nA : cA + (size_t)(t + 2) * kstep; const char* b2 = last ? nB : cB + (size_t)(t + 2) * kstep;
;             const char* a3 = a2 + kstep; const char* b3 = b2 + kstep;
;             if (last && has_next) S.a_ready(nxt);
;             if constexpr (SP2) {
;             PG8_LDB(B0, 0, 0); PG8_LDB(B1, 0, 1); PG8_SCHED; PG8_LDA(At, 0, 0); PG8_STAGE(PG8_SA(1, 1), a1 + hstep, voffA);
;             PG8_WAIT_V(8); PG8_WAIT_L(0); PG8_BAR; PG8_MMA(0, 0, At, B0); PG8_MMA(0, 1, At, B1); PG8_BAR; PG8_SCHED;
;             PG8_LDA(At, 0, 1); PG8_STAGE(PG8_SB(0, 0), b2, voffB); PG8_STAGE(PG8_SB(0, 1), b2 + hstepB, voffB); PG8_STAGE(PG8_SA(0, 0), a2, voffA);
;             PG8_WAIT_V(8); PG8_WAIT_L(0); PG8_BAR; PG8_MMA(1, 0, At, B0); PG8_MMA(1, 1, At, B1); PG8_BAR; PG8_SCHED;
.LBB0_984:
	s_add_i32 s75, s42, 2
	v_add_u32_e32 v186, s59, v173
	v_add_u32_e32 v202, s61, v173
	s_add_u32 s0, s38, s40
	ds_read_b128 v[168:171], v186
	ds_read_b128 v[178:181], v186 offset:1024
	ds_read_b128 v[182:185], v186 offset:2048
	ds_read_b128 v[186:189], v186 offset:3072
	ds_read_b128 v[190:193], v202
	ds_read_b128 v[194:197], v202 offset:1024
	ds_read_b128 v[198:201], v202 offset:2048
	ds_read_b128 v[202:205], v202 offset:3072
	s_addc_u32 s1, s39, s41
	s_add_u32 s0, s0, 0x100
	s_addc_u32 s1, s1, 0
	s_add_u32 s33, s73, s40
	s_addc_u32 s76, s74, s41
	s_cmp_eq_u32 s57, s42
	s_cselect_b32 s43, s3, s1
	s_cselect_b32 s42, s2, s0
	s_cselect_b32 s1, s37, s76
	s_cselect_b32 s0, s36, s33
	v_lshl_add_u64 v[240:241], v[164:165], 0, s[40:41]
	s_add_i32 m0, s47, 0xc000
	ds_read_b128 v[206:209], v176
	ds_read_b128 v[212:215], v176 offset:1024
	ds_read_b128 v[216:219], v176 offset:2048
	ds_read_b128 v[220:223], v176 offset:3072
	ds_read_b128 v[224:227], v176 offset:4096
	ds_read_b128 v[228:231], v176 offset:5120
	ds_read_b128 v[232:235], v176 offset:6144
	ds_read_b128 v[236:239], v176 offset:7168
	global_load_lds_dwordx4 v[240:241], off
	v_lshl_add_u64 v[240:241], v[166:167], 0, s[40:41]
	s_add_i32 m0, s47, 0xe000
	s_nop 0
	global_load_lds_dwordx4 v[240:241], off
	s_waitcnt vmcnt(8)
	s_waitcnt lgkmcnt(0)
	s_setprio 1
	s_barrier
	v_mfma_f32_16x16x32_bf16 v[126:129], v[168:171], v[206:209], v[126:129]
	v_mfma_f32_16x16x32_bf16 v[122:125], v[182:185], v[206:209], v[122:125]
	v_mfma_f32_16x16x32_bf16 v[110:113], v[168:171], v[216:219], v[110:113]
	v_mfma_f32_16x16x32_bf16 v[106:109], v[182:185], v[216:219], v[106:109]
	v_mfma_f32_16x16x32_bf16 v[94:97], v[168:171], v[224:227], v[94:97]
	v_mfma_f32_16x16x32_bf16 v[90:93], v[182:185], v[224:227], v[90:93]
	v_mfma_f32_16x16x32_bf16 v[78:81], v[168:171], v[232:235], v[78:81]
	v_mfma_f32_16x16x32_bf16 v[74:77], v[182:185], v[232:235], v[74:77]
	v_mfma_f32_16x16x32_bf16 v[126:129], v[178:181], v[212:215], v[126:129]
	v_mfma_f32_16x16x32_bf16 v[122:125], v[186:189], v[212:215], v[122:125]
	v_mfma_f32_16x16x32_bf16 v[110:113], v[178:181], v[220:223], v[110:113]
	v_mfma_f32_16x16x32_bf16 v[106:109], v[186:189], v[220:223], v[106:109]
	v_mfma_f32_16x16x32_bf16 v[94:97], v[178:181], v[228:231], v[94:97]
	v_mfma_f32_16x16x32_bf16 v[90:93], v[186:189], v[228:231], v[90:93]
	v_mfma_f32_16x16x32_bf16 v[78:81], v[178:181], v[236:239], v[78:81]
	v_mfma_f32_16x16x32_bf16 v[74:77], v[186:189], v[236:239], v[74:77]
	v_mfma_f32_16x16x32_bf16 v[118:121], v[190:193], v[206:209], v[118:121]
	v_mfma_f32_16x16x32_bf16 v[114:117], v[198:201], v[206:209], v[114:117]
	v_mfma_f32_16x16x32_bf16 v[102:105], v[190:193], v[216:219], v[102:105]
	v_mfma_f32_16x16x32_bf16 v[98:101], v[198:201], v[216:219], v[98:101]
	v_mfma_f32_16x16x32_bf16 v[86:89], v[190:193], v[224:227], v[86:89]
	v_mfma_f32_16x16x32_bf16 v[82:85], v[198:201], v[224:227], v[82:85]
	v_mfma_f32_16x16x32_bf16 v[70:73], v[190:193], v[232:235], v[70:73]
	v_mfma_f32_16x16x32_bf16 v[66:69], v[198:201], v[232:235], v[66:69]
	v_mfma_f32_16x16x32_bf16 v[118:121], v[194:197], v[212:215], v[118:121]
	v_mfma_f32_16x16x32_bf16 v[114:117], v[202:205], v[212:215], v[114:117]
	v_mfma_f32_16x16x32_bf16 v[102:105], v[194:197], v[220:223], v[102:105]
	v_mfma_f32_16x16x32_bf16 v[98:101], v[202:205], v[220:223], v[98:101]
	v_mfma_f32_16x16x32_bf16 v[86:89], v[194:197], v[228:231], v[86:89]
	v_mfma_f32_16x16x32_bf16 v[82:85], v[202:205], v[228:231], v[82:85]
	v_mfma_f32_16x16x32_bf16 v[70:73], v[194:197], v[236:239], v[70:73]
	v_mfma_f32_16x16x32_bf16 v[66:69], v[202:205], v[236:239], v[66:69]
	s_setprio 0
	s_barrier
	s_add_i32 s33, s59, s46
	v_lshl_add_u64 v[240:241], s[0:1], 0, v[132:133]
	s_mov_b32 m0, s33
	ds_read_b128 v[206:209], v176 offset:16384
	ds_read_b128 v[212:215], v176 offset:17408
	ds_read_b128 v[216:219], v176 offset:18432
	ds_read_b128 v[220:223], v176 offset:19456
	ds_read_b128 v[224:227], v176 offset:20480
	ds_read_b128 v[228:231], v176 offset:21504
	ds_read_b128 v[232:235], v176 offset:22528
	ds_read_b128 v[236:239], v176 offset:23552
	global_load_lds_dwordx4 v[240:241], off
	s_add_i32 m0, s33, 0x2000
	v_lshl_add_u64 v[242:243], s[0:1], 0, v[136:137]
	s_add_u32 s0, s0, s14
	s_addc_u32 s1, s1, s15
	s_add_i32 s33, s61, s46
	global_load_lds_dwordx4 v[242:243], off
	v_lshl_add_u64 v[244:245], s[0:1], 0, v[132:133]
	s_mov_b32 m0, s33
	v_lshl_add_u64 v[246:247], s[0:1], 0, v[136:137]
	global_load_lds_dwordx4 v[244:245], off
	s_add_i32 m0, s33, 0x2000
	v_lshl_add_u64 v[248:249], s[42:43], 0, v[130:131]
	global_load_lds_dwordx4 v[246:247], off
	v_lshl_add_u64 v[250:251], s[42:43], 0, v[134:135]
	s_waitcnt vmcnt(6)
	s_waitcnt lgkmcnt(0)
	s_setprio 1
	s_barrier
; #define PG8_STAGE(bufoff, gbase, voff) do { _Pragma("unroll") for (int _i = 0; _i < 2; ++_i) \
;         __builtin_amdgcn_global_load_lds((const unsigned*)((const char*)(gbase) + (voff)[_i]), (PG8_LAS unsigned*)(lds + (bufoff) + ldsw + _i * 8192), 16, 0, 0); } while (0)
; #define PG8_LDA(dst, b, h) do { _Pragma("unroll") for (int m = 0; m < 4; ++m) { const bf16x8 f0_ = *(const PG8_LAS bf16x8*)(lds + PG8_SA(b, h) + aoff + m * 2048), f1_ = *(const PG8_LAS bf16x8*)(lds + PG8_SA(b, h) + aoff + m * 2048 + 1024); dst[m].set(f0_, f1_); } } while (0)
; #define PG8_LDB(dst, b, h) do { _Pragma("unroll") for (int n = 0; n < 2; ++n) { const bf16x8 f0_ = *(const PG8_LAS bf16x8*)(lds + PG8_SB(b, h) + boff + n * 2048), f1_ = *(const PG8_LAS bf16x8*)(lds + PG8_SB(b, h) + boff + n * 2048 + 1024); dst[n].set(f0_, f1_); } } while (0)
; #define PG8_WAIT_V(n) asm volatile("s_waitcnt vmcnt(" #n ")" ::: "memory")
; #define PG8_WAIT_L(n) asm volatile("s_waitcnt lgkmcnt(" #n ")" ::: "memory")
; #define PG8_BAR __builtin_amdgcn_s_barrier()
; #define PG8_SCHED __builtin_amdgcn_sched_barrier(0)
; template <class Epi, class Sched, bool ALIGN_EPI = false, bool SP2 = false>
; __device__ __forceinline__ void gemm_phase(PG8_LAS unsigned char* lds, const Gemm g, const Sched& S, const Epi& E) {
;     ...
;             PG8_WAIT_V(8); PG8_WAIT_L(0); PG8_BAR; PG8_MMA(1, 0, At, B0); PG8_MMA(1, 1, At, B1); PG8_BAR; PG8_SCHED;
;             PG8_LDB(B0, 1, 0); PG8_LDB(B1, 1, 1); PG8_SCHED; PG8_LDA(At, 1, 0); PG8_STAGE(PG8_SA(0, 1), a2 + hstep, voffA);
;             PG8_WAIT_V(8); PG8_WAIT_L(0); PG8_BAR; PG8_MMA(0, 0, At, B0); PG8_MMA(0, 1, At, B1); PG8_BAR; PG8_SCHED;
	v_mfma_f32_16x16x32_bf16 v[62:65], v[168:171], v[206:209], v[62:65]
	v_mfma_f32_16x16x32_bf16 v[58:61], v[182:185], v[206:209], v[58:61]
	v_mfma_f32_16x16x32_bf16 v[46:49], v[168:171], v[216:219], v[46:49]
	v_mfma_f32_16x16x32_bf16 v[42:45], v[182:185], v[216:219], v[42:45]
	v_mfma_f32_16x16x32_bf16 v[30:33], v[168:171], v[224:227], v[30:33]
	v_mfma_f32_16x16x32_bf16 v[26:29], v[182:185], v[224:227], v[26:29]
	v_mfma_f32_16x16x32_bf16 v[14:17], v[168:171], v[232:235], v[14:17]
	v_mfma_f32_16x16x32_bf16 v[10:13], v[182:185], v[232:235], v[10:13]
	v_mfma_f32_16x16x32_bf16 v[62:65], v[178:181], v[212:215], v[62:65]
	v_mfma_f32_16x16x32_bf16 v[58:61], v[186:189], v[212:215], v[58:61]
	v_mfma_f32_16x16x32_bf16 v[46:49], v[178:181], v[220:223], v[46:49]
	v_mfma_f32_16x16x32_bf16 v[42:45], v[186:189], v[220:223], v[42:45]
	v_mfma_f32_16x16x32_bf16 v[30:33], v[178:181], v[228:231], v[30:33]
	v_mfma_f32_16x16x32_bf16 v[26:29], v[186:189], v[228:231], v[26:29]
	v_mfma_f32_16x16x32_bf16 v[14:17], v[178:181], v[236:239], v[14:17]
	v_mfma_f32_16x16x32_bf16 v[10:13], v[186:189], v[236:239], v[10:13]
	v_mfma_f32_16x16x32_bf16 v[54:57], v[190:193], v[206:209], v[54:57]
	v_mfma_f32_16x16x32_bf16 v[50:53], v[198:201], v[206:209], v[50:53]
	v_mfma_f32_16x16x32_bf16 v[38:41], v[190:193], v[216:219], v[38:41]
	v_mfma_f32_16x16x32_bf16 v[34:37], v[198:201], v[216:219], v[34:37]
	v_mfma_f32_16x16x32_bf16 v[22:25], v[190:193], v[224:227], v[22:25]
	v_mfma_f32_16x16x32_bf16 v[18:21], v[198:201], v[224:227], v[18:21]
	v_mfma_f32_16x16x32_bf16 v[6:9], v[190:193], v[232:235], v[6:9]
	v_mfma_f32_16x16x32_bf16 v[2:5], v[198:201], v[232:235], v[2:5]
	v_mfma_f32_16x16x32_bf16 v[54:57], v[194:197], v[212:215], v[54:57]
	v_mfma_f32_16x16x32_bf16 v[50:53], v[202:205], v[212:215], v[50:53]
	v_mfma_f32_16x16x32_bf16 v[38:41], v[194:197], v[220:223], v[38:41]
	v_mfma_f32_16x16x32_bf16 v[34:37], v[202:205], v[220:223], v[34:37]
	v_mfma_f32_16x16x32_bf16 v[22:25], v[194:197], v[228:231], v[22:25]
	v_mfma_f32_16x16x32_bf16 v[18:21], v[202:205], v[228:231], v[18:21]
	v_mfma_f32_16x16x32_bf16 v[6:9], v[194:197], v[236:239], v[6:9]
	v_mfma_f32_16x16x32_bf16 v[2:5], v[202:205], v[236:239], v[2:5]
	s_setprio 0
	s_barrier
	s_add_i32 s33, 0, 0x18000
	s_add_i32 s76, 0, 0x1c000
	v_add_u32_e32 v186, s33, v173
	v_add_u32_e32 v202, s76, v173
	ds_read_b128 v[168:171], v186
	ds_read_b128 v[178:181], v186 offset:1024
	ds_read_b128 v[182:185], v186 offset:2048
	ds_read_b128 v[186:189], v186 offset:3072
	ds_read_b128 v[190:193], v202
	ds_read_b128 v[194:197], v202 offset:1024
	ds_read_b128 v[198:201], v202 offset:2048
	ds_read_b128 v[202:205], v202 offset:3072
	s_add_u32 s0, s42, s12
	s_addc_u32 s1, s43, s13
	s_mov_b32 m0, s49
	v_lshl_add_u64 v[252:253], s[0:1], 0, v[130:131]
	ds_read_b128 v[206:209], v176 offset:32768
	ds_read_b128 v[212:215], v176 offset:33792
	ds_read_b128 v[216:219], v176 offset:34816
	ds_read_b128 v[220:223], v176 offset:35840
	ds_read_b128 v[224:227], v176 offset:36864
	ds_read_b128 v[228:231], v176 offset:37888
	ds_read_b128 v[232:235], v176 offset:38912
	ds_read_b128 v[236:239], v176 offset:39936
	s_mov_b32 m0, s47
	s_nop 0
	global_load_lds_dwordx4 v[248:249], off
	s_mov_b32 m0, s48
	s_nop 0
	global_load_lds_dwordx4 v[250:251], off
	s_mov_b32 m0, s49
	s_nop 0
	global_load_lds_dwordx4 v[252:253], off
	v_lshl_add_u64 v[252:253], s[0:1], 0, v[134:135]
	s_mov_b32 m0, s50
	s_nop 0
	global_load_lds_dwordx4 v[252:253], off
	s_waitcnt vmcnt(8)
	s_waitcnt lgkmcnt(0)
	s_setprio 1
	s_barrier
; #define PG8_STAGE(bufoff, gbase, voff) do { _Pragma("unroll") for (int _i = 0; _i < 2; ++_i) \
;         __builtin_amdgcn_global_load_lds((const unsigned*)((const char*)(gbase) + (voff)[_i]), (PG8_LAS unsigned*)(lds + (bufoff) + ldsw + _i * 8192), 16, 0, 0); } while (0)
; #define PG8_LDA(dst, b, h) do { _Pragma("unroll") for (int m = 0; m < 4; ++m) { const bf16x8 f0_ = *(const PG8_LAS bf16x8*)(lds + PG8_SA(b, h) + aoff + m * 2048), f1_ = *(const PG8_LAS bf16x8*)(lds + PG8_SA(b, h) + aoff + m * 2048 + 1024); dst[m].set(f0_, f1_); } } while (0)
; #define PG8_WAIT_V(n) asm volatile("s_waitcnt vmcnt(" #n ")" ::: "memory")
; #define PG8_WAIT_L(n) asm volatile("s_waitcnt lgkmcnt(" #n ")" ::: "memory")
; #define PG8_BAR __builtin_amdgcn_s_barrier()
; #define PG8_SCHED __builtin_amdgcn_sched_barrier(0)
; template <class Epi, class Sched, bool ALIGN_EPI = false, bool SP2 = false>
; __device__ __forceinline__ void gemm_phase(PG8_LAS unsigned char* lds, const Gemm g, const Sched& S, const Epi& E) {
;     ...
;             PG8_WAIT_V(8); PG8_WAIT_L(0); PG8_BAR; PG8_MMA(0, 0, At, B0); PG8_MMA(0, 1, At, B1); PG8_BAR; PG8_SCHED;
;             PG8_LDA(At, 1, 1); PG8_STAGE(PG8_SB(1, 0), b3, voffB); PG8_STAGE(PG8_SB(1, 1), b3 + hstepB, voffB); PG8_STAGE(PG8_SA(1, 0), a3, voffA);
;             PG8_WAIT_V(8); PG8_WAIT_L(0); PG8_BAR; PG8_MMA(1, 0, At, B0); PG8_MMA(1, 1, At, B1); PG8_BAR; PG8_SCHED;
	v_mfma_f32_16x16x32_bf16 v[126:129], v[168:171], v[206:209], v[126:129]
	v_mfma_f32_16x16x32_bf16 v[122:125], v[182:185], v[206:209], v[122:125]
	v_mfma_f32_16x16x32_bf16 v[110:113], v[168:171], v[216:219], v[110:113]
	v_mfma_f32_16x16x32_bf16 v[106:109], v[182:185], v[216:219], v[106:109]
	v_mfma_f32_16x16x32_bf16 v[94:97], v[168:171], v[224:227], v[94:97]
	v_mfma_f32_16x16x32_bf16 v[90:93], v[182:185], v[224:227], v[90:93]
	v_mfma_f32_16x16x32_bf16 v[78:81], v[168:171], v[232:235], v[78:81]
	v_mfma_f32_16x16x32_bf16 v[74:77], v[182:185], v[232:235], v[74:77]
	v_mfma_f32_16x16x32_bf16 v[126:129], v[178:181], v[212:215], v[126:129]
	v_mfma_f32_16x16x32_bf16 v[122:125], v[186:189], v[212:215], v[122:125]
	v_mfma_f32_16x16x32_bf16 v[110:113], v[178:181], v[220:223], v[110:113]
	v_mfma_f32_16x16x32_bf16 v[106:109], v[186:189], v[220:223], v[106:109]
	v_mfma_f32_16x16x32_bf16 v[94:97], v[178:181], v[228:231], v[94:97]
	v_mfma_f32_16x16x32_bf16 v[90:93], v[186:189], v[228:231], v[90:93]
	v_mfma_f32_16x16x32_bf16 v[78:81], v[178:181], v[236:239], v[78:81]
	v_mfma_f32_16x16x32_bf16 v[74:77], v[186:189], v[236:239], v[74:77]
	v_mfma_f32_16x16x32_bf16 v[118:121], v[190:193], v[206:209], v[118:121]
	v_mfma_f32_16x16x32_bf16 v[114:117], v[198:201], v[206:209], v[114:117]
	v_mfma_f32_16x16x32_bf16 v[102:105], v[190:193], v[216:219], v[102:105]
	v_mfma_f32_16x16x32_bf16 v[98:101], v[198:201], v[216:219], v[98:101]
	v_mfma_f32_16x16x32_bf16 v[86:89], v[190:193], v[224:227], v[86:89]
	v_mfma_f32_16x16x32_bf16 v[82:85], v[198:201], v[224:227], v[82:85]
	v_mfma_f32_16x16x32_bf16 v[70:73], v[190:193], v[232:235], v[70:73]
	v_mfma_f32_16x16x32_bf16 v[66:69], v[198:201], v[232:235], v[66:69]
	v_mfma_f32_16x16x32_bf16 v[118:121], v[194:197], v[212:215], v[118:121]
	v_mfma_f32_16x16x32_bf16 v[114:117], v[202:205], v[212:215], v[114:117]
	v_mfma_f32_16x16x32_bf16 v[102:105], v[194:197], v[220:223], v[102:105]
	v_mfma_f32_16x16x32_bf16 v[98:101], v[202:205], v[220:223], v[98:101]
	v_mfma_f32_16x16x32_bf16 v[86:89], v[194:197], v[228:231], v[86:89]
	v_mfma_f32_16x16x32_bf16 v[82:85], v[202:205], v[228:231], v[82:85]
	v_mfma_f32_16x16x32_bf16 v[70:73], v[194:197], v[236:239], v[70:73]
	v_mfma_f32_16x16x32_bf16 v[66:69], v[202:205], v[236:239], v[66:69]
	s_setprio 0
	s_barrier
	s_add_i32 s0, s33, s46
	v_lshl_add_u64 v[240:241], v[240:241], 0, s[26:27]
	s_mov_b32 m0, s0
	ds_read_b128 v[206:209], v176 offset:49152
	ds_read_b128 v[212:215], v176 offset:50176
	ds_read_b128 v[216:219], v176 offset:51200
	ds_read_b128 v[220:223], v176 offset:52224
	ds_read_b128 v[224:227], v176 offset:53248
	ds_read_b128 v[228:231], v176 offset:54272
	ds_read_b128 v[232:235], v176 offset:55296
	ds_read_b128 v[236:239], v176 offset:56320
	global_load_lds_dwordx4 v[240:241], off
	v_lshl_add_u64 v[240:241], v[242:243], 0, s[26:27]
	s_add_i32 m0, s0, 0x2000
	s_add_i32 s0, s76, s46
	global_load_lds_dwordx4 v[240:241], off
	v_lshl_add_u64 v[240:241], v[244:245], 0, s[26:27]
	s_mov_b32 m0, s0
	s_nop 0
	global_load_lds_dwordx4 v[240:241], off
	v_lshl_add_u64 v[240:241], v[246:247], 0, s[26:27]
	s_add_i32 m0, s0, 0x2000
	s_nop 0
	global_load_lds_dwordx4 v[240:241], off
	v_lshl_add_u64 v[240:241], v[248:249], 0, s[26:27]
	s_mov_b32 m0, s52
	s_nop 0
	global_load_lds_dwordx4 v[240:241], off
	v_lshl_add_u64 v[240:241], v[250:251], 0, s[26:27]
	s_mov_b32 m0, s53
	s_nop 0
	global_load_lds_dwordx4 v[240:241], off
	s_waitcnt vmcnt(6)
	s_waitcnt lgkmcnt(0)
	s_setprio 1
	s_barrier
	v_mfma_f32_16x16x32_bf16 v[62:65], v[168:171], v[206:209], v[62:65]
	v_mfma_f32_16x16x32_bf16 v[58:61], v[182:185], v[206:209], v[58:61]
	v_mfma_f32_16x16x32_bf16 v[46:49], v[168:171], v[216:219], v[46:49]
	v_mfma_f32_16x16x32_bf16 v[42:45], v[182:185], v[216:219], v[42:45]
	v_mfma_f32_16x16x32_bf16 v[30:33], v[168:171], v[224:227], v[30:33]
	v_mfma_f32_16x16x32_bf16 v[26:29], v[182:185], v[224:227], v[26:29]
	v_mfma_f32_16x16x32_bf16 v[14:17], v[168:171], v[232:235], v[14:17]
	v_mfma_f32_16x16x32_bf16 v[10:13], v[182:185], v[232:235], v[10:13]
	v_mfma_f32_16x16x32_bf16 v[62:65], v[178:181], v[212:215], v[62:65]
	v_mfma_f32_16x16x32_bf16 v[58:61], v[186:189], v[212:215], v[58:61]
	v_mfma_f32_16x16x32_bf16 v[46:49], v[178:181], v[220:223], v[46:49]
	v_mfma_f32_16x16x32_bf16 v[42:45], v[186:189], v[220:223], v[42:45]
	v_mfma_f32_16x16x32_bf16 v[30:33], v[178:181], v[228:231], v[30:33]
	v_mfma_f32_16x16x32_bf16 v[26:29], v[186:189], v[228:231], v[26:29]
	v_mfma_f32_16x16x32_bf16 v[14:17], v[178:181], v[236:239], v[14:17]
	v_mfma_f32_16x16x32_bf16 v[10:13], v[186:189], v[236:239], v[10:13]
	v_mfma_f32_16x16x32_bf16 v[54:57], v[190:193], v[206:209], v[54:57]
	v_mfma_f32_16x16x32_bf16 v[50:53], v[198:201], v[206:209], v[50:53]
	v_mfma_f32_16x16x32_bf16 v[38:41], v[190:193], v[216:219], v[38:41]
	v_mfma_f32_16x16x32_bf16 v[34:37], v[198:201], v[216:219], v[34:37]
	v_mfma_f32_16x16x32_bf16 v[22:25], v[190:193], v[224:227], v[22:25]
	v_mfma_f32_16x16x32_bf16 v[18:21], v[198:201], v[224:227], v[18:21]
	v_mfma_f32_16x16x32_bf16 v[6:9], v[190:193], v[232:235], v[6:9]
	v_mfma_f32_16x16x32_bf16 v[2:5], v[198:201], v[232:235], v[2:5]
	v_mfma_f32_16x16x32_bf16 v[54:57], v[194:197], v[212:215], v[54:57]
	v_mfma_f32_16x16x32_bf16 v[50:53], v[202:205], v[212:215], v[50:53]
	v_mfma_f32_16x16x32_bf16 v[38:41], v[194:197], v[220:223], v[38:41]
	v_mfma_f32_16x16x32_bf16 v[34:37], v[202:205], v[220:223], v[34:37]
	v_mfma_f32_16x16x32_bf16 v[22:25], v[194:197], v[228:231], v[22:25]
	v_mfma_f32_16x16x32_bf16 v[18:21], v[202:205], v[228:231], v[18:21]
	v_mfma_f32_16x16x32_bf16 v[6:9], v[194:197], v[236:239], v[6:9]
	v_mfma_f32_16x16x32_bf16 v[2:5], v[202:205], v[236:239], v[2:5]
	s_setprio 0
	s_barrier
	s_add_u32 s40, s40, 0x100
	s_addc_u32 s41, s41, 0
	s_cmp_ge_i32 s75, s54
	s_cbranch_scc0 .LBB0_982

; #define PG8_STAGE(bufoff, gbase, voff) do { _Pragma("unroll") for (int _i = 0; _i < 2; ++_i) \
;         __builtin_amdgcn_global_load_lds((const unsigned*)((const char*)(gbase) + (voff)[_i]), (PG8_LAS unsigned*)(lds + (bufoff) + ldsw + _i * 8192), 16, 0, 0); } while (0)
; #define PG8_LDA(dst, b, h) do { _Pragma("unroll") for (int m = 0; m < 4; ++m) { const bf16x8 f0_ = *(const PG8_LAS bf16x8*)(lds + PG8_SA(b, h) + aoff + m * 2048), f1_ = *(const PG8_LAS bf16x8*)(lds + PG8_SA(b, h) + aoff + m * 2048 + 1024); dst[m].set(f0_, f1_); } } while (0)
; #define PG8_LDB(dst, b, h) do { _Pragma("unroll") for (int n = 0; n < 2; ++n) { const bf16x8 f0_ = *(const PG8_LAS bf16x8*)(lds + PG8_SB(b, h) + boff + n * 2048), f1_ = *(const PG8_LAS bf16x8*)(lds + PG8_SB(b, h) + boff + n * 2048 + 1024); dst[n].set(f0_, f1_); } } while (0)
; #define PG8_WAIT_V(n) asm volatile("s_waitcnt vmcnt(" #n ")" ::: "memory")
; #define PG8_WAIT_L(n) asm volatile("s_waitcnt lgkmcnt(" #n ")" ::: "memory")
; #define PG8_BAR __builtin_amdgcn_s_barrier()
; #define PG8_SCHED __builtin_amdgcn_sched_barrier(0)
; template <class Epi, class Sched, bool ALIGN_EPI = false, bool SP2 = false>
; __device__ __forceinline__ void gemm_phase(PG8_LAS unsigned char* lds, const Gemm g, const Sched& S, const Epi& E) {
;     ...
;             PG8_LDB(B0, 0, 0); PG8_LDB(B1, 0, 1); PG8_SCHED; PG8_LDA(At, 0, 0); PG8_STAGE(PG8_SA(1, 1), a1 + hstep, voffA);
;             PG8_WAIT_V(8); PG8_WAIT_L(0); PG8_BAR; PG8_MMA(0, 0, At, B0); PG8_MMA(0, 1, At, B1); PG8_BAR; PG8_SCHED;
;             PG8_LDA(At, 0, 1); PG8_STAGE(PG8_SB(0, 0), b2, voffB); PG8_STAGE(PG8_SB(0, 1), b2 + hstepB, voffB); PG8_STAGE(PG8_SA(0, 0), a2, voffA);
;             PG8_WAIT_V(8); PG8_WAIT_L(0); PG8_BAR; PG8_MMA(1, 0, At, B0); PG8_MMA(1, 1, At, B1); PG8_BAR; PG8_SCHED;
.Lkr2_a:
	v_lshl_add_u64 v[224:225], s[56:57], 0, v[176:177]
	s_add_i32 m0, s67, 0xc000
	ds_read_b128 v[162:165], v195
	ds_read_b128 v[186:189], v195 offset:1024
	ds_read_b128 v[198:201], v195 offset:2048
	ds_read_b128 v[202:205], v195 offset:3072
	ds_read_b128 v[206:209], v195 offset:4096
	ds_read_b128 v[212:215], v195 offset:5120
	ds_read_b128 v[216:219], v195 offset:6144
	ds_read_b128 v[220:223], v195 offset:7168
	global_load_lds_dwordx4 v[224:225], off
	v_lshl_add_u64 v[224:225], s[56:57], 0, v[178:179]
	s_add_i32 m0, s67, 0xe000
	s_nop 0
	global_load_lds_dwordx4 v[224:225], off
	s_waitcnt vmcnt(8)
	s_waitcnt lgkmcnt(0)
	s_setprio 1
	s_barrier
	v_mfma_f32_16x16x32_bf16 v[126:129], v[130:133], v[162:165], v[126:129]
	v_mfma_f32_16x16x32_bf16 v[122:125], v[138:141], v[162:165], v[122:125]
	v_mfma_f32_16x16x32_bf16 v[58:61], v[130:133], v[198:201], v[58:61]
	v_mfma_f32_16x16x32_bf16 v[62:65], v[138:141], v[198:201], v[62:65]
	v_mfma_f32_16x16x32_bf16 v[106:109], v[130:133], v[206:209], v[106:109]
	v_mfma_f32_16x16x32_bf16 v[110:113], v[138:141], v[206:209], v[110:113]
	v_mfma_f32_16x16x32_bf16 v[98:101], v[130:133], v[216:219], v[98:101]
	v_mfma_f32_16x16x32_bf16 v[102:105], v[138:141], v[216:219], v[102:105]
	v_mfma_f32_16x16x32_bf16 v[126:129], v[134:137], v[186:189], v[126:129]
	v_mfma_f32_16x16x32_bf16 v[122:125], v[142:145], v[186:189], v[122:125]
	v_mfma_f32_16x16x32_bf16 v[58:61], v[134:137], v[202:205], v[58:61]
	v_mfma_f32_16x16x32_bf16 v[62:65], v[142:145], v[202:205], v[62:65]
	v_mfma_f32_16x16x32_bf16 v[106:109], v[134:137], v[212:215], v[106:109]
	v_mfma_f32_16x16x32_bf16 v[110:113], v[142:145], v[212:215], v[110:113]
	v_mfma_f32_16x16x32_bf16 v[98:101], v[134:137], v[220:223], v[98:101]
	v_mfma_f32_16x16x32_bf16 v[102:105], v[142:145], v[220:223], v[102:105]
	v_mfma_f32_16x16x32_bf16 v[118:121], v[146:149], v[162:165], v[118:121]
	v_mfma_f32_16x16x32_bf16 v[114:117], v[154:157], v[162:165], v[114:117]
	v_mfma_f32_16x16x32_bf16 v[50:53], v[146:149], v[198:201], v[50:53]
	v_mfma_f32_16x16x32_bf16 v[54:57], v[154:157], v[198:201], v[54:57]
	v_mfma_f32_16x16x32_bf16 v[90:93], v[146:149], v[206:209], v[90:93]
	v_mfma_f32_16x16x32_bf16 v[94:97], v[154:157], v[206:209], v[94:97]
	v_mfma_f32_16x16x32_bf16 v[74:77], v[146:149], v[216:219], v[74:77]
	v_mfma_f32_16x16x32_bf16 v[78:81], v[154:157], v[216:219], v[78:81]
	v_mfma_f32_16x16x32_bf16 v[118:121], v[150:153], v[186:189], v[118:121]
	v_mfma_f32_16x16x32_bf16 v[114:117], v[158:161], v[186:189], v[114:117]
	v_mfma_f32_16x16x32_bf16 v[50:53], v[150:153], v[202:205], v[50:53]
	v_mfma_f32_16x16x32_bf16 v[54:57], v[158:161], v[202:205], v[54:57]
	v_mfma_f32_16x16x32_bf16 v[90:93], v[150:153], v[212:215], v[90:93]
	v_mfma_f32_16x16x32_bf16 v[94:97], v[158:161], v[212:215], v[94:97]
	v_mfma_f32_16x16x32_bf16 v[74:77], v[150:153], v[220:223], v[74:77]
	v_mfma_f32_16x16x32_bf16 v[78:81], v[158:161], v[220:223], v[78:81]
	s_setprio 0
	s_barrier
	s_add_i32 s33, s82, s66
	v_lshl_add_u64 v[224:225], s[0:1], 0, v[168:169]
	s_mov_b32 m0, s33
	ds_read_b128 v[162:165], v195 offset:16384
	ds_read_b128 v[186:189], v195 offset:17408
	ds_read_b128 v[198:201], v195 offset:18432
	ds_read_b128 v[202:205], v195 offset:19456
	ds_read_b128 v[206:209], v195 offset:20480
	ds_read_b128 v[212:215], v195 offset:21504
	ds_read_b128 v[216:219], v195 offset:22528
	ds_read_b128 v[220:223], v195 offset:23552
	global_load_lds_dwordx4 v[224:225], off
	s_add_i32 m0, s33, 0x2000
	v_lshl_add_u64 v[226:227], s[0:1], 0, v[172:173]
	s_add_u32 s0, s0, s16
	s_addc_u32 s1, s1, s17
	s_add_i32 s33, s83, s66
	global_load_lds_dwordx4 v[226:227], off
	v_lshl_add_u64 v[228:229], s[0:1], 0, v[168:169]
	s_mov_b32 m0, s33
	v_lshl_add_u64 v[230:231], s[0:1], 0, v[172:173]
	global_load_lds_dwordx4 v[228:229], off
	s_add_i32 m0, s33, 0x2000
	v_lshl_add_u64 v[232:233], s[58:59], 0, v[166:167]
	global_load_lds_dwordx4 v[230:231], off
	v_lshl_add_u64 v[234:235], s[58:59], 0, v[170:171]
	s_waitcnt vmcnt(6)
	s_waitcnt lgkmcnt(0)
	s_setprio 1
	s_barrier
	v_mfma_f32_16x16x32_bf16 v[82:85], v[130:133], v[162:165], v[82:85]
	v_mfma_f32_16x16x32_bf16 v[86:89], v[138:141], v[162:165], v[86:89]
	v_mfma_f32_16x16x32_bf16 v[46:49], v[130:133], v[198:201], v[46:49]
	v_mfma_f32_16x16x32_bf16 v[42:45], v[138:141], v[198:201], v[42:45]
	v_mfma_f32_16x16x32_bf16 v[30:33], v[130:133], v[206:209], v[30:33]
	v_mfma_f32_16x16x32_bf16 v[26:29], v[138:141], v[206:209], v[26:29]
	v_mfma_f32_16x16x32_bf16 v[14:17], v[130:133], v[216:219], v[14:17]
	v_mfma_f32_16x16x32_bf16 v[6:9], v[138:141], v[216:219], v[6:9]
	v_mfma_f32_16x16x32_bf16 v[82:85], v[134:137], v[186:189], v[82:85]
	v_mfma_f32_16x16x32_bf16 v[86:89], v[142:145], v[186:189], v[86:89]
	v_mfma_f32_16x16x32_bf16 v[46:49], v[134:137], v[202:205], v[46:49]
	v_mfma_f32_16x16x32_bf16 v[42:45], v[142:145], v[202:205], v[42:45]
	v_mfma_f32_16x16x32_bf16 v[30:33], v[134:137], v[212:215], v[30:33]
	v_mfma_f32_16x16x32_bf16 v[26:29], v[142:145], v[212:215], v[26:29]
	v_mfma_f32_16x16x32_bf16 v[14:17], v[134:137], v[220:223], v[14:17]
	v_mfma_f32_16x16x32_bf16 v[6:9], v[142:145], v[220:223], v[6:9]
	v_mfma_f32_16x16x32_bf16 v[66:69], v[146:149], v[162:165], v[66:69]
	v_mfma_f32_16x16x32_bf16 v[70:73], v[154:157], v[162:165], v[70:73]
	v_mfma_f32_16x16x32_bf16 v[38:41], v[146:149], v[198:201], v[38:41]
	v_mfma_f32_16x16x32_bf16 v[34:37], v[154:157], v[198:201], v[34:37]
	v_mfma_f32_16x16x32_bf16 v[22:25], v[146:149], v[206:209], v[22:25]
	v_mfma_f32_16x16x32_bf16 v[18:21], v[154:157], v[206:209], v[18:21]
	v_mfma_f32_16x16x32_bf16 v[10:13], v[146:149], v[216:219], v[10:13]
	v_mfma_f32_16x16x32_bf16 v[2:5], v[154:157], v[216:219], v[2:5]
	v_mfma_f32_16x16x32_bf16 v[66:69], v[150:153], v[186:189], v[66:69]
	v_mfma_f32_16x16x32_bf16 v[70:73], v[158:161], v[186:189], v[70:73]
	v_mfma_f32_16x16x32_bf16 v[38:41], v[150:153], v[202:205], v[38:41]
	v_mfma_f32_16x16x32_bf16 v[34:37], v[158:161], v[202:205], v[34:37]
	v_mfma_f32_16x16x32_bf16 v[22:25], v[150:153], v[212:215], v[22:25]
	v_mfma_f32_16x16x32_bf16 v[18:21], v[158:161], v[212:215], v[18:21]
	v_mfma_f32_16x16x32_bf16 v[10:13], v[150:153], v[220:223], v[10:13]
	v_mfma_f32_16x16x32_bf16 v[2:5], v[158:161], v[220:223], v[2:5]
	s_setprio 0
	s_barrier
; #define PG8_STAGE(bufoff, gbase, voff) do { _Pragma("unroll") for (int _i = 0; _i < 2; ++_i) \
;         __builtin_amdgcn_global_load_lds((const unsigned*)((const char*)(gbase) + (voff)[_i]), (PG8_LAS unsigned*)(lds + (bufoff) + ldsw + _i * 8192), 16, 0, 0); } while (0)
; #define PG8_LDA(dst, b, h) do { _Pragma("unroll") for (int m = 0; m < 4; ++m) { const bf16x8 f0_ = *(const PG8_LAS bf16x8*)(lds + PG8_SA(b, h) + aoff + m * 2048), f1_ = *(const PG8_LAS bf16x8*)(lds + PG8_SA(b, h) + aoff + m * 2048 + 1024); dst[m].set(f0_, f1_); } } while (0)
; #define PG8_LDB(dst, b, h) do { _Pragma("unroll") for (int n = 0; n < 2; ++n) { const bf16x8 f0_ = *(const PG8_LAS bf16x8*)(lds + PG8_SB(b, h) + boff + n * 2048), f1_ = *(const PG8_LAS bf16x8*)(lds + PG8_SB(b, h) + boff + n * 2048 + 1024); dst[n].set(f0_, f1_); } } while (0)
; #define PG8_WAIT_V(n) asm volatile("s_waitcnt vmcnt(" #n ")" ::: "memory")
; #define PG8_WAIT_L(n) asm volatile("s_waitcnt lgkmcnt(" #n ")" ::: "memory")
; #define PG8_BAR __builtin_amdgcn_s_barrier()
; #define PG8_SCHED __builtin_amdgcn_sched_barrier(0)
; template <class Epi, class Sched, bool ALIGN_EPI = false, bool SP2 = false>
; __device__ __forceinline__ void gemm_phase(PG8_LAS unsigned char* lds, const Gemm g, const Sched& S, const Epi& E) {
;     ...
;             PG8_LDB(B0, 1, 0); PG8_LDB(B1, 1, 1); PG8_SCHED; PG8_LDA(At, 1, 0); PG8_STAGE(PG8_SA(0, 1), a2 + hstep, voffA);
;             PG8_WAIT_V(8); PG8_WAIT_L(0); PG8_BAR; PG8_MMA(0, 0, At, B0); PG8_MMA(0, 1, At, B1); PG8_BAR; PG8_SCHED;
;             PG8_LDA(At, 1, 1); PG8_STAGE(PG8_SB(1, 0), b3, voffB); PG8_STAGE(PG8_SB(1, 1), b3 + hstepB, voffB); PG8_STAGE(PG8_SA(1, 0), a3, voffA);
	s_add_i32 s33, 0, 0x18000
	s_add_i32 s96, 0, 0x1c000
	v_add_u32_e32 v142, s33, v190
	v_add_u32_e32 v158, s96, v190
	ds_read_b128 v[130:133], v142
	ds_read_b128 v[134:137], v142 offset:1024
	ds_read_b128 v[138:141], v142 offset:2048
	ds_read_b128 v[142:145], v142 offset:3072
	ds_read_b128 v[146:149], v158
	ds_read_b128 v[150:153], v158 offset:1024
	ds_read_b128 v[154:157], v158 offset:2048
	ds_read_b128 v[158:161], v158 offset:3072
	s_add_u32 s0, s58, s14
	s_addc_u32 s1, s59, s15
	s_mov_b32 m0, s71
	v_lshl_add_u64 v[236:237], s[0:1], 0, v[166:167]
	ds_read_b128 v[162:165], v195 offset:32768
	ds_read_b128 v[186:189], v195 offset:33792
	ds_read_b128 v[198:201], v195 offset:34816
	ds_read_b128 v[202:205], v195 offset:35840
	ds_read_b128 v[206:209], v195 offset:36864
	ds_read_b128 v[212:215], v195 offset:37888
	ds_read_b128 v[216:219], v195 offset:38912
	ds_read_b128 v[220:223], v195 offset:39936
	s_mov_b32 m0, s67
	s_nop 0
	global_load_lds_dwordx4 v[232:233], off
	s_mov_b32 m0, s69
	s_nop 0
	global_load_lds_dwordx4 v[234:235], off
	s_mov_b32 m0, s71
	s_nop 0
	global_load_lds_dwordx4 v[236:237], off
	v_lshl_add_u64 v[236:237], s[0:1], 0, v[170:171]
	s_mov_b32 m0, s73
	s_nop 0
	global_load_lds_dwordx4 v[236:237], off
	s_waitcnt vmcnt(8)
	s_waitcnt lgkmcnt(0)
	s_setprio 1
	s_barrier
	v_mfma_f32_16x16x32_bf16 v[126:129], v[130:133], v[162:165], v[126:129]
	v_mfma_f32_16x16x32_bf16 v[122:125], v[138:141], v[162:165], v[122:125]
	v_mfma_f32_16x16x32_bf16 v[58:61], v[130:133], v[198:201], v[58:61]
	v_mfma_f32_16x16x32_bf16 v[62:65], v[138:141], v[198:201], v[62:65]
	v_mfma_f32_16x16x32_bf16 v[106:109], v[130:133], v[206:209], v[106:109]
	v_mfma_f32_16x16x32_bf16 v[110:113], v[138:141], v[206:209], v[110:113]
	v_mfma_f32_16x16x32_bf16 v[98:101], v[130:133], v[216:219], v[98:101]
	v_mfma_f32_16x16x32_bf16 v[102:105], v[138:141], v[216:219], v[102:105]
	v_mfma_f32_16x16x32_bf16 v[126:129], v[134:137], v[186:189], v[126:129]
	v_mfma_f32_16x16x32_bf16 v[122:125], v[142:145], v[186:189], v[122:125]
	v_mfma_f32_16x16x32_bf16 v[58:61], v[134:137], v[202:205], v[58:61]
	v_mfma_f32_16x16x32_bf16 v[62:65], v[142:145], v[202:205], v[62:65]
	v_mfma_f32_16x16x32_bf16 v[106:109], v[134:137], v[212:215], v[106:109]
	v_mfma_f32_16x16x32_bf16 v[110:113], v[142:145], v[212:215], v[110:113]
	v_mfma_f32_16x16x32_bf16 v[98:101], v[134:137], v[220:223], v[98:101]
	v_mfma_f32_16x16x32_bf16 v[102:105], v[142:145], v[220:223], v[102:105]
	v_mfma_f32_16x16x32_bf16 v[118:121], v[146:149], v[162:165], v[118:121]
	v_mfma_f32_16x16x32_bf16 v[114:117], v[154:157], v[162:165], v[114:117]
	v_mfma_f32_16x16x32_bf16 v[50:53], v[146:149], v[198:201], v[50:53]
	v_mfma_f32_16x16x32_bf16 v[54:57], v[154:157], v[198:201], v[54:57]
	v_mfma_f32_16x16x32_bf16 v[90:93], v[146:149], v[206:209], v[90:93]
	v_mfma_f32_16x16x32_bf16 v[94:97], v[154:157], v[206:209], v[94:97]
	v_mfma_f32_16x16x32_bf16 v[74:77], v[146:149], v[216:219], v[74:77]
	v_mfma_f32_16x16x32_bf16 v[78:81], v[154:157], v[216:219], v[78:81]
	v_mfma_f32_16x16x32_bf16 v[118:121], v[150:153], v[186:189], v[118:121]
	v_mfma_f32_16x16x32_bf16 v[114:117], v[158:161], v[186:189], v[114:117]
	v_mfma_f32_16x16x32_bf16 v[50:53], v[150:153], v[202:205], v[50:53]
	v_mfma_f32_16x16x32_bf16 v[54:57], v[158:161], v[202:205], v[54:57]
	v_mfma_f32_16x16x32_bf16 v[90:93], v[150:153], v[212:215], v[90:93]
	v_mfma_f32_16x16x32_bf16 v[94:97], v[158:161], v[212:215], v[94:97]
	v_mfma_f32_16x16x32_bf16 v[74:77], v[150:153], v[220:223], v[74:77]
	v_mfma_f32_16x16x32_bf16 v[78:81], v[158:161], v[220:223], v[78:81]
	s_setprio 0
	s_barrier
	s_add_i32 s0, s33, s66
	v_lshl_add_u64 v[224:225], v[224:225], 0, s[28:29]
	s_mov_b32 m0, s0
	ds_read_b128 v[162:165], v195 offset:49152
	ds_read_b128 v[186:189], v195 offset:50176
	ds_read_b128 v[198:201], v195 offset:51200
	ds_read_b128 v[202:205], v195 offset:52224
	ds_read_b128 v[206:209], v195 offset:53248
	ds_read_b128 v[212:215], v195 offset:54272
	ds_read_b128 v[216:219], v195 offset:55296
	ds_read_b128 v[220:223], v195 offset:56320
	global_load_lds_dwordx4 v[224:225], off
	v_lshl_add_u64 v[224:225], v[226:227], 0, s[28:29]
	s_add_i32 m0, s0, 0x2000
	s_add_i32 s0, s96, s66
	global_load_lds_dwordx4 v[224:225], off
	v_lshl_add_u64 v[224:225], v[228:229], 0, s[28:29]
	s_mov_b32 m0, s0
	s_nop 0
	global_load_lds_dwordx4 v[224:225], off
	v_lshl_add_u64 v[224:225], v[230:231], 0, s[28:29]
	s_add_i32 m0, s0, 0x2000
	s_nop 0
	global_load_lds_dwordx4 v[224:225], off
	s_cmp_ge_i32 s95, s76
	s_cbranch_scc0 .Lkr2_b
	v_lshl_add_u64 v[224:225], v[232:233], 0, s[28:29]
	s_mov_b32 m0, s74
	s_nop 0
	global_load_lds_dwordx4 v[224:225], off
	v_lshl_add_u64 v[224:225], v[234:235], 0, s[28:29]
	s_mov_b32 m0, s75
	s_nop 0
	global_load_lds_dwordx4 v[224:225], off
; #define PG8_WAIT_V(n) asm volatile("s_waitcnt vmcnt(" #n ")" ::: "memory")
; #define PG8_WAIT_L(n) asm volatile("s_waitcnt lgkmcnt(" #n ")" ::: "memory")
; #define PG8_BAR __builtin_amdgcn_s_barrier()
; #define PG8_SCHED __builtin_amdgcn_sched_barrier(0)
; template <class Epi, class Sched, bool ALIGN_EPI = false, bool SP2 = false>
; __device__ __forceinline__ void gemm_phase(PG8_LAS unsigned char* lds, const Gemm g, const Sched& S, const Epi& E) {
;     ...
;         for (int t = 0; t < nt; t += 2) {
;             if constexpr (Epi::MIDK) { if (t == (nt >> 1)) E.mid(acc, cur, wr, wc, fr, fq); }
;             const bool last = (t == nt - 2);
;             const char* a1 = cA + (size_t)(t + 1) * kstep;
;             const char* a2 = last ? nA : cA + (size_t)(t + 2) * kstep; const char* b2 = last ? nB : cB + (size_t)(t + 2) * kstep;
;             const char* a3 = a2 + kstep; const char* b3 = b2 + kstep;
;     ...
;             PG8_WAIT_V(8); PG8_WAIT_L(0); PG8_BAR; PG8_MMA(1, 0, At, B0); PG8_MMA(1, 1, At, B1); PG8_BAR; PG8_SCHED;
.Lkr2_b:
	s_waitcnt vmcnt(6)
	s_waitcnt lgkmcnt(0)
	s_setprio 1
	s_barrier
	v_mfma_f32_16x16x32_bf16 v[82:85], v[130:133], v[162:165], v[82:85]
	v_mfma_f32_16x16x32_bf16 v[86:89], v[138:141], v[162:165], v[86:89]
	v_mfma_f32_16x16x32_bf16 v[46:49], v[130:133], v[198:201], v[46:49]
	v_mfma_f32_16x16x32_bf16 v[42:45], v[138:141], v[198:201], v[42:45]
	v_mfma_f32_16x16x32_bf16 v[30:33], v[130:133], v[206:209], v[30:33]
	v_mfma_f32_16x16x32_bf16 v[26:29], v[138:141], v[206:209], v[26:29]
	v_mfma_f32_16x16x32_bf16 v[14:17], v[130:133], v[216:219], v[14:17]
	v_mfma_f32_16x16x32_bf16 v[6:9], v[138:141], v[216:219], v[6:9]
	v_mfma_f32_16x16x32_bf16 v[82:85], v[134:137], v[186:189], v[82:85]
	v_mfma_f32_16x16x32_bf16 v[86:89], v[142:145], v[186:189], v[86:89]
	v_mfma_f32_16x16x32_bf16 v[46:49], v[134:137], v[202:205], v[46:49]
	v_mfma_f32_16x16x32_bf16 v[42:45], v[142:145], v[202:205], v[42:45]
	v_mfma_f32_16x16x32_bf16 v[30:33], v[134:137], v[212:215], v[30:33]
	v_mfma_f32_16x16x32_bf16 v[26:29], v[142:145], v[212:215], v[26:29]
	v_mfma_f32_16x16x32_bf16 v[14:17], v[134:137], v[220:223], v[14:17]
	v_mfma_f32_16x16x32_bf16 v[6:9], v[142:145], v[220:223], v[6:9]
	v_mfma_f32_16x16x32_bf16 v[66:69], v[146:149], v[162:165], v[66:69]
	v_mfma_f32_16x16x32_bf16 v[70:73], v[154:157], v[162:165], v[70:73]
	v_mfma_f32_16x16x32_bf16 v[38:41], v[146:149], v[198:201], v[38:41]
	v_mfma_f32_16x16x32_bf16 v[34:37], v[154:157], v[198:201], v[34:37]
	v_mfma_f32_16x16x32_bf16 v[22:25], v[146:149], v[206:209], v[22:25]
	v_mfma_f32_16x16x32_bf16 v[18:21], v[154:157], v[206:209], v[18:21]
	v_mfma_f32_16x16x32_bf16 v[10:13], v[146:149], v[216:219], v[10:13]
	v_mfma_f32_16x16x32_bf16 v[2:5], v[154:157], v[216:219], v[2:5]
	v_mfma_f32_16x16x32_bf16 v[66:69], v[150:153], v[186:189], v[66:69]
	v_mfma_f32_16x16x32_bf16 v[70:73], v[158:161], v[186:189], v[70:73]
	v_mfma_f32_16x16x32_bf16 v[38:41], v[150:153], v[202:205], v[38:41]
	v_mfma_f32_16x16x32_bf16 v[34:37], v[158:161], v[202:205], v[34:37]
	v_mfma_f32_16x16x32_bf16 v[22:25], v[150:153], v[212:215], v[22:25]
	v_mfma_f32_16x16x32_bf16 v[18:21], v[158:161], v[212:215], v[18:21]
	v_mfma_f32_16x16x32_bf16 v[10:13], v[150:153], v[220:223], v[10:13]
	v_mfma_f32_16x16x32_bf16 v[2:5], v[158:161], v[220:223], v[2:5]
	s_setprio 0
	s_barrier
	s_add_u32 s56, s56, 0x100
	s_addc_u32 s57, s57, 0
	s_add_u32 s93, s93, 0x100
	s_addc_u32 s94, s94, 0
	s_cmp_ge_i32 s95, s76
	s_cselect_b32 s99, 0, 1
	s_mov_b32 s58, s95
	s_cbranch_scc0 .LBB0_1070
	v_readlane_b32 s94, v254, 5
	v_readlane_b32 s95, v254, 6

; #define PG8_STAGE(bufoff, gbase, voff) do { _Pragma("unroll") for (int _i = 0; _i < 2; ++_i) \
;         __builtin_amdgcn_global_load_lds((const unsigned*)((const char*)(gbase) + (voff)[_i]), (PG8_LAS unsigned*)(lds + (bufoff) + ldsw + _i * 8192), 16, 0, 0); } while (0)
; #define PG8_LDA(dst, b, h) do { _Pragma("unroll") for (int m = 0; m < 4; ++m) { const bf16x8 f0_ = *(const PG8_LAS bf16x8*)(lds + PG8_SA(b, h) + aoff + m * 2048), f1_ = *(const PG8_LAS bf16x8*)(lds + PG8_SA(b, h) + aoff + m * 2048 + 1024); dst[m].set(f0_, f1_); } } while (0)
; #define PG8_LDB(dst, b, h) do { _Pragma("unroll") for (int n = 0; n < 2; ++n) { const bf16x8 f0_ = *(const PG8_LAS bf16x8*)(lds + PG8_SB(b, h) + boff + n * 2048), f1_ = *(const PG8_LAS bf16x8*)(lds + PG8_SB(b, h) + boff + n * 2048 + 1024); dst[n].set(f0_, f1_); } } while (0)
; #define PG8_WAIT_V(n) asm volatile("s_waitcnt vmcnt(" #n ")" ::: "memory")
; #define PG8_WAIT_L(n) asm volatile("s_waitcnt lgkmcnt(" #n ")" ::: "memory")
; #define PG8_BAR __builtin_amdgcn_s_barrier()
; #define PG8_SCHED __builtin_amdgcn_sched_barrier(0)
; template <class Epi, class Sched, bool ALIGN_EPI = false, bool SP2 = false>
; __device__ __forceinline__ void gemm_phase(PG8_LAS unsigned char* lds, const Gemm g, const Sched& S, const Epi& E) {
;     ...
;             PG8_LDB(B0, 0, 0); PG8_LDB(B1, 0, 1); PG8_SCHED; PG8_LDA(At, 0, 0); PG8_STAGE(PG8_SA(1, 1), a1 + hstep, voffA);
;             PG8_WAIT_V(8); PG8_WAIT_L(0); PG8_BAR; PG8_MMA(0, 0, At, B0); PG8_MMA(0, 1, At, B1); PG8_BAR; PG8_SCHED;
;             PG8_LDA(At, 0, 1); PG8_STAGE(PG8_SB(0, 0), b2, voffB); PG8_STAGE(PG8_SB(0, 1), b2 + hstepB, voffB); PG8_STAGE(PG8_SA(0, 0), a2, voffA);
;             PG8_WAIT_V(8); PG8_WAIT_L(0); PG8_BAR; PG8_MMA(1, 0, At, B0); PG8_MMA(1, 1, At, B1); PG8_BAR; PG8_SCHED;
.Lkr3_a:
	v_lshl_add_u64 v[148:149], s[30:31], 0, v[140:141]
	s_add_i32 m0, s40, 0xc000
	ds_read_b128 v[188:191], v154
	ds_read_b128 v[192:195], v154 offset:1024
	ds_read_b128 v[196:199], v154 offset:2048
	ds_read_b128 v[200:203], v154 offset:3072
	ds_read_b128 v[204:207], v154 offset:4096
	ds_read_b128 v[212:215], v154 offset:5120
	ds_read_b128 v[216:219], v154 offset:6144
	ds_read_b128 v[220:223], v154 offset:7168
	global_load_lds_dwordx4 v[148:149], off
	v_lshl_add_u64 v[148:149], s[30:31], 0, v[142:143]
	s_add_i32 m0, s40, 0xe000
	s_nop 0
	global_load_lds_dwordx4 v[148:149], off
	s_waitcnt vmcnt(8)
	s_waitcnt lgkmcnt(0)
	s_setprio 1
	s_barrier
	v_mfma_f32_16x16x32_bf16 v[126:129], v[156:159], v[188:191], v[126:129]
	v_mfma_f32_16x16x32_bf16 v[122:125], v[164:167], v[188:191], v[122:125]
	v_mfma_f32_16x16x32_bf16 v[110:113], v[156:159], v[196:199], v[110:113]
	v_mfma_f32_16x16x32_bf16 v[106:109], v[164:167], v[196:199], v[106:109]
	v_mfma_f32_16x16x32_bf16 v[94:97], v[156:159], v[204:207], v[94:97]
	v_mfma_f32_16x16x32_bf16 v[90:93], v[164:167], v[204:207], v[90:93]
	v_mfma_f32_16x16x32_bf16 v[78:81], v[156:159], v[216:219], v[78:81]
	v_mfma_f32_16x16x32_bf16 v[74:77], v[164:167], v[216:219], v[74:77]
	v_mfma_f32_16x16x32_bf16 v[126:129], v[160:163], v[192:195], v[126:129]
	v_mfma_f32_16x16x32_bf16 v[122:125], v[168:171], v[192:195], v[122:125]
	v_mfma_f32_16x16x32_bf16 v[110:113], v[160:163], v[200:203], v[110:113]
	v_mfma_f32_16x16x32_bf16 v[106:109], v[168:171], v[200:203], v[106:109]
	v_mfma_f32_16x16x32_bf16 v[94:97], v[160:163], v[212:215], v[94:97]
	v_mfma_f32_16x16x32_bf16 v[90:93], v[168:171], v[212:215], v[90:93]
	v_mfma_f32_16x16x32_bf16 v[78:81], v[160:163], v[220:223], v[78:81]
	v_mfma_f32_16x16x32_bf16 v[74:77], v[168:171], v[220:223], v[74:77]
	v_mfma_f32_16x16x32_bf16 v[118:121], v[172:175], v[188:191], v[118:121]
	v_mfma_f32_16x16x32_bf16 v[114:117], v[180:183], v[188:191], v[114:117]
	v_mfma_f32_16x16x32_bf16 v[102:105], v[172:175], v[196:199], v[102:105]
	v_mfma_f32_16x16x32_bf16 v[98:101], v[180:183], v[196:199], v[98:101]
	v_mfma_f32_16x16x32_bf16 v[86:89], v[172:175], v[204:207], v[86:89]
	v_mfma_f32_16x16x32_bf16 v[82:85], v[180:183], v[204:207], v[82:85]
	v_mfma_f32_16x16x32_bf16 v[70:73], v[172:175], v[216:219], v[70:73]
	v_mfma_f32_16x16x32_bf16 v[66:69], v[180:183], v[216:219], v[66:69]
	v_mfma_f32_16x16x32_bf16 v[118:121], v[176:179], v[192:195], v[118:121]
	v_mfma_f32_16x16x32_bf16 v[114:117], v[184:187], v[192:195], v[114:117]
	v_mfma_f32_16x16x32_bf16 v[102:105], v[176:179], v[200:203], v[102:105]
	v_mfma_f32_16x16x32_bf16 v[98:101], v[184:187], v[200:203], v[98:101]
	v_mfma_f32_16x16x32_bf16 v[86:89], v[176:179], v[212:215], v[86:89]
	v_mfma_f32_16x16x32_bf16 v[82:85], v[184:187], v[212:215], v[82:85]
	v_mfma_f32_16x16x32_bf16 v[70:73], v[176:179], v[220:223], v[70:73]
	v_mfma_f32_16x16x32_bf16 v[66:69], v[184:187], v[220:223], v[66:69]
	s_setprio 0
	s_barrier
	s_add_i32 s33, s52, s39
	v_lshl_add_u64 v[148:149], s[0:1], 0, v[132:133]
	s_mov_b32 m0, s33
	ds_read_b128 v[188:191], v154 offset:16384
	ds_read_b128 v[192:195], v154 offset:17408
	ds_read_b128 v[196:199], v154 offset:18432
	ds_read_b128 v[200:203], v154 offset:19456
	ds_read_b128 v[204:207], v154 offset:20480
	ds_read_b128 v[212:215], v154 offset:21504
	ds_read_b128 v[216:219], v154 offset:22528
	ds_read_b128 v[220:223], v154 offset:23552
	global_load_lds_dwordx4 v[148:149], off
	s_add_i32 m0, s33, 0x2000
	v_lshl_add_u64 v[208:209], s[0:1], 0, v[136:137]
	s_add_u32 s0, s0, s14
	s_addc_u32 s1, s1, s15
	s_add_i32 s33, s53, s39
	global_load_lds_dwordx4 v[208:209], off
	v_lshl_add_u64 v[224:225], s[0:1], 0, v[132:133]
	s_mov_b32 m0, s33
	v_lshl_add_u64 v[226:227], s[0:1], 0, v[136:137]
	global_load_lds_dwordx4 v[224:225], off
	s_add_i32 m0, s33, 0x2000
	v_lshl_add_u64 v[228:229], s[34:35], 0, v[130:131]
	global_load_lds_dwordx4 v[226:227], off
	v_lshl_add_u64 v[230:231], s[34:35], 0, v[134:135]
	s_waitcnt vmcnt(6)
	s_waitcnt lgkmcnt(0)
	s_setprio 1
	s_barrier
	v_mfma_f32_16x16x32_bf16 v[62:65], v[156:159], v[188:191], v[62:65]
	v_mfma_f32_16x16x32_bf16 v[58:61], v[164:167], v[188:191], v[58:61]
	v_mfma_f32_16x16x32_bf16 v[46:49], v[156:159], v[196:199], v[46:49]
	v_mfma_f32_16x16x32_bf16 v[42:45], v[164:167], v[196:199], v[42:45]
	v_mfma_f32_16x16x32_bf16 v[30:33], v[156:159], v[204:207], v[30:33]
	v_mfma_f32_16x16x32_bf16 v[26:29], v[164:167], v[204:207], v[26:29]
	v_mfma_f32_16x16x32_bf16 v[14:17], v[156:159], v[216:219], v[14:17]
	v_mfma_f32_16x16x32_bf16 v[6:9], v[164:167], v[216:219], v[6:9]
	v_mfma_f32_16x16x32_bf16 v[62:65], v[160:163], v[192:195], v[62:65]
	v_mfma_f32_16x16x32_bf16 v[58:61], v[168:171], v[192:195], v[58:61]
	v_mfma_f32_16x16x32_bf16 v[46:49], v[160:163], v[200:203], v[46:49]
	v_mfma_f32_16x16x32_bf16 v[42:45], v[168:171], v[200:203], v[42:45]
	v_mfma_f32_16x16x32_bf16 v[30:33], v[160:163], v[212:215], v[30:33]
	v_mfma_f32_16x16x32_bf16 v[26:29], v[168:171], v[212:215], v[26:29]
	v_mfma_f32_16x16x32_bf16 v[14:17], v[160:163], v[220:223], v[14:17]
	v_mfma_f32_16x16x32_bf16 v[6:9], v[168:171], v[220:223], v[6:9]
	v_mfma_f32_16x16x32_bf16 v[54:57], v[172:175], v[188:191], v[54:57]
	v_mfma_f32_16x16x32_bf16 v[50:53], v[180:183], v[188:191], v[50:53]
	v_mfma_f32_16x16x32_bf16 v[38:41], v[172:175], v[196:199], v[38:41]
	v_mfma_f32_16x16x32_bf16 v[34:37], v[180:183], v[196:199], v[34:37]
	v_mfma_f32_16x16x32_bf16 v[22:25], v[172:175], v[204:207], v[22:25]
	v_mfma_f32_16x16x32_bf16 v[18:21], v[180:183], v[204:207], v[18:21]
	v_mfma_f32_16x16x32_bf16 v[10:13], v[172:175], v[216:219], v[10:13]
	v_mfma_f32_16x16x32_bf16 v[2:5], v[180:183], v[216:219], v[2:5]
	v_mfma_f32_16x16x32_bf16 v[54:57], v[176:179], v[192:195], v[54:57]
	v_mfma_f32_16x16x32_bf16 v[50:53], v[184:187], v[192:195], v[50:53]
	v_mfma_f32_16x16x32_bf16 v[38:41], v[176:179], v[200:203], v[38:41]
	v_mfma_f32_16x16x32_bf16 v[34:37], v[184:187], v[200:203], v[34:37]
	v_mfma_f32_16x16x32_bf16 v[22:25], v[176:179], v[212:215], v[22:25]
	v_mfma_f32_16x16x32_bf16 v[18:21], v[184:187], v[212:215], v[18:21]
	v_mfma_f32_16x16x32_bf16 v[10:13], v[176:179], v[220:223], v[10:13]
	v_mfma_f32_16x16x32_bf16 v[2:5], v[184:187], v[220:223], v[2:5]
	s_setprio 0
	s_barrier
; #define PG8_STAGE(bufoff, gbase, voff) do { _Pragma("unroll") for (int _i = 0; _i < 2; ++_i) \
;         __builtin_amdgcn_global_load_lds((const unsigned*)((const char*)(gbase) + (voff)[_i]), (PG8_LAS unsigned*)(lds + (bufoff) + ldsw + _i * 8192), 16, 0, 0); } while (0)
; #define PG8_LDA(dst, b, h) do { _Pragma("unroll") for (int m = 0; m < 4; ++m) { const bf16x8 f0_ = *(const PG8_LAS bf16x8*)(lds + PG8_SA(b, h) + aoff + m * 2048), f1_ = *(const PG8_LAS bf16x8*)(lds + PG8_SA(b, h) + aoff + m * 2048 + 1024); dst[m].set(f0_, f1_); } } while (0)
; #define PG8_LDB(dst, b, h) do { _Pragma("unroll") for (int n = 0; n < 2; ++n) { const bf16x8 f0_ = *(const PG8_LAS bf16x8*)(lds + PG8_SB(b, h) + boff + n * 2048), f1_ = *(const PG8_LAS bf16x8*)(lds + PG8_SB(b, h) + boff + n * 2048 + 1024); dst[n].set(f0_, f1_); } } while (0)
; #define PG8_WAIT_V(n) asm volatile("s_waitcnt vmcnt(" #n ")" ::: "memory")
; #define PG8_WAIT_L(n) asm volatile("s_waitcnt lgkmcnt(" #n ")" ::: "memory")
; #define PG8_BAR __builtin_amdgcn_s_barrier()
; #define PG8_SCHED __builtin_amdgcn_sched_barrier(0)
; template <class Epi, class Sched, bool ALIGN_EPI = false, bool SP2 = false>
; __device__ __forceinline__ void gemm_phase(PG8_LAS unsigned char* lds, const Gemm g, const Sched& S, const Epi& E) {
;     ...
;             PG8_LDB(B0, 1, 0); PG8_LDB(B1, 1, 1); PG8_SCHED; PG8_LDA(At, 1, 0); PG8_STAGE(PG8_SA(0, 1), a2 + hstep, voffA);
;             PG8_WAIT_V(8); PG8_WAIT_L(0); PG8_BAR; PG8_MMA(0, 0, At, B0); PG8_MMA(0, 1, At, B1); PG8_BAR; PG8_SCHED;
;             PG8_LDA(At, 1, 1); PG8_STAGE(PG8_SB(1, 0), b3, voffB); PG8_STAGE(PG8_SB(1, 1), b3 + hstepB, voffB); PG8_STAGE(PG8_SA(1, 0), a3, voffA);
	s_add_i32 s33, 0, 0x18000
	s_add_i32 s63, 0, 0x1c000
	v_add_u32_e32 v168, s33, v1
	v_add_u32_e32 v184, s63, v1
	ds_read_b128 v[156:159], v168
	ds_read_b128 v[160:163], v168 offset:1024
	ds_read_b128 v[164:167], v168 offset:2048
	ds_read_b128 v[168:171], v168 offset:3072
	ds_read_b128 v[172:175], v184
	ds_read_b128 v[176:179], v184 offset:1024
	ds_read_b128 v[180:183], v184 offset:2048
	ds_read_b128 v[184:187], v184 offset:3072
	s_add_u32 s0, s34, s12
	s_addc_u32 s1, s35, s13
	s_mov_b32 m0, s42
	v_lshl_add_u64 v[232:233], s[0:1], 0, v[130:131]
	ds_read_b128 v[188:191], v154 offset:32768
	ds_read_b128 v[192:195], v154 offset:33792
	ds_read_b128 v[196:199], v154 offset:34816
	ds_read_b128 v[200:203], v154 offset:35840
	ds_read_b128 v[204:207], v154 offset:36864
	ds_read_b128 v[212:215], v154 offset:37888
	ds_read_b128 v[216:219], v154 offset:38912
	ds_read_b128 v[220:223], v154 offset:39936
	s_mov_b32 m0, s40
	s_nop 0
	global_load_lds_dwordx4 v[228:229], off
	s_mov_b32 m0, s41
	s_nop 0
	global_load_lds_dwordx4 v[230:231], off
	s_mov_b32 m0, s42
	s_nop 0
	global_load_lds_dwordx4 v[232:233], off
	v_lshl_add_u64 v[232:233], s[0:1], 0, v[134:135]
	s_mov_b32 m0, s43
	s_nop 0
	global_load_lds_dwordx4 v[232:233], off
	s_waitcnt vmcnt(8)
	s_waitcnt lgkmcnt(0)
	s_setprio 1
	s_barrier
	v_mfma_f32_16x16x32_bf16 v[126:129], v[156:159], v[188:191], v[126:129]
	v_mfma_f32_16x16x32_bf16 v[122:125], v[164:167], v[188:191], v[122:125]
	v_mfma_f32_16x16x32_bf16 v[110:113], v[156:159], v[196:199], v[110:113]
	v_mfma_f32_16x16x32_bf16 v[106:109], v[164:167], v[196:199], v[106:109]
	v_mfma_f32_16x16x32_bf16 v[94:97], v[156:159], v[204:207], v[94:97]
	v_mfma_f32_16x16x32_bf16 v[90:93], v[164:167], v[204:207], v[90:93]
	v_mfma_f32_16x16x32_bf16 v[78:81], v[156:159], v[216:219], v[78:81]
	v_mfma_f32_16x16x32_bf16 v[74:77], v[164:167], v[216:219], v[74:77]
	v_mfma_f32_16x16x32_bf16 v[126:129], v[160:163], v[192:195], v[126:129]
	v_mfma_f32_16x16x32_bf16 v[122:125], v[168:171], v[192:195], v[122:125]
	v_mfma_f32_16x16x32_bf16 v[110:113], v[160:163], v[200:203], v[110:113]
	v_mfma_f32_16x16x32_bf16 v[106:109], v[168:171], v[200:203], v[106:109]
	v_mfma_f32_16x16x32_bf16 v[94:97], v[160:163], v[212:215], v[94:97]
	v_mfma_f32_16x16x32_bf16 v[90:93], v[168:171], v[212:215], v[90:93]
	v_mfma_f32_16x16x32_bf16 v[78:81], v[160:163], v[220:223], v[78:81]
	v_mfma_f32_16x16x32_bf16 v[74:77], v[168:171], v[220:223], v[74:77]
	v_mfma_f32_16x16x32_bf16 v[118:121], v[172:175], v[188:191], v[118:121]
	v_mfma_f32_16x16x32_bf16 v[114:117], v[180:183], v[188:191], v[114:117]
	v_mfma_f32_16x16x32_bf16 v[102:105], v[172:175], v[196:199], v[102:105]
	v_mfma_f32_16x16x32_bf16 v[98:101], v[180:183], v[196:199], v[98:101]
	v_mfma_f32_16x16x32_bf16 v[86:89], v[172:175], v[204:207], v[86:89]
	v_mfma_f32_16x16x32_bf16 v[82:85], v[180:183], v[204:207], v[82:85]
	v_mfma_f32_16x16x32_bf16 v[70:73], v[172:175], v[216:219], v[70:73]
	v_mfma_f32_16x16x32_bf16 v[66:69], v[180:183], v[216:219], v[66:69]
	v_mfma_f32_16x16x32_bf16 v[118:121], v[176:179], v[192:195], v[118:121]
	v_mfma_f32_16x16x32_bf16 v[114:117], v[184:187], v[192:195], v[114:117]
	v_mfma_f32_16x16x32_bf16 v[102:105], v[176:179], v[200:203], v[102:105]
	v_mfma_f32_16x16x32_bf16 v[98:101], v[184:187], v[200:203], v[98:101]
	v_mfma_f32_16x16x32_bf16 v[86:89], v[176:179], v[212:215], v[86:89]
	v_mfma_f32_16x16x32_bf16 v[82:85], v[184:187], v[212:215], v[82:85]
	v_mfma_f32_16x16x32_bf16 v[70:73], v[176:179], v[220:223], v[70:73]
	v_mfma_f32_16x16x32_bf16 v[66:69], v[184:187], v[220:223], v[66:69]
	s_setprio 0
	s_barrier
	s_add_i32 s0, s33, s39
	v_lshl_add_u64 v[148:149], v[148:149], 0, s[22:23]
	s_mov_b32 m0, s0
	ds_read_b128 v[188:191], v154 offset:49152
	ds_read_b128 v[192:195], v154 offset:50176
	ds_read_b128 v[196:199], v154 offset:51200
	ds_read_b128 v[200:203], v154 offset:52224
	ds_read_b128 v[204:207], v154 offset:53248
	ds_read_b128 v[212:215], v154 offset:54272
	ds_read_b128 v[216:219], v154 offset:55296
	ds_read_b128 v[220:223], v154 offset:56320
	global_load_lds_dwordx4 v[148:149], off
	v_lshl_add_u64 v[148:149], v[208:209], 0, s[22:23]
	s_add_i32 m0, s0, 0x2000
	s_add_i32 s0, s63, s39
	global_load_lds_dwordx4 v[148:149], off
	v_lshl_add_u64 v[148:149], v[224:225], 0, s[22:23]
	s_mov_b32 m0, s0
	s_nop 0
	global_load_lds_dwordx4 v[148:149], off
	v_lshl_add_u64 v[148:149], v[226:227], 0, s[22:23]
	s_add_i32 m0, s0, 0x2000
	s_nop 0
	global_load_lds_dwordx4 v[148:149], off
	s_cmp_ge_i32 s61, s47
	s_cbranch_scc0 .Lkr3_b
	v_lshl_add_u64 v[148:149], v[228:229], 0, s[22:23]
	s_mov_b32 m0, s45
	s_nop 0
	global_load_lds_dwordx4 v[148:149], off
	v_lshl_add_u64 v[148:149], v[230:231], 0, s[22:23]
	s_mov_b32 m0, s46
	s_nop 0
	global_load_lds_dwordx4 v[148:149], off
; #define PG8_WAIT_V(n) asm volatile("s_waitcnt vmcnt(" #n ")" ::: "memory")
; #define PG8_WAIT_L(n) asm volatile("s_waitcnt lgkmcnt(" #n ")" ::: "memory")
; #define PG8_BAR __builtin_amdgcn_s_barrier()
; #define PG8_SCHED __builtin_amdgcn_sched_barrier(0)
; template <class Epi, class Sched, bool ALIGN_EPI = false, bool SP2 = false>
; __device__ __forceinline__ void gemm_phase(PG8_LAS unsigned char* lds, const Gemm g, const Sched& S, const Epi& E) {
;     ...
;         for (int t = 0; t < nt; t += 2) {
;             if constexpr (Epi::MIDK) { if (t == (nt >> 1)) E.mid(acc, cur, wr, wc, fr, fq); }
;             const bool last = (t == nt - 2);
;             const char* a1 = cA + (size_t)(t + 1) * kstep;
;             const char* a2 = last ? nA : cA + (size_t)(t + 2) * kstep; const char* b2 = last ? nB : cB + (size_t)(t + 2) * kstep;
;             const char* a3 = a2 + kstep; const char* b3 = b2 + kstep;
;     ...
;             PG8_WAIT_V(8); PG8_WAIT_L(0); PG8_BAR; PG8_MMA(1, 0, At, B0); PG8_MMA(1, 1, At, B1); PG8_BAR; PG8_SCHED;
.Lkr3_b:
	s_waitcnt vmcnt(6)
	s_waitcnt lgkmcnt(0)
	s_setprio 1
	s_barrier
	v_mfma_f32_16x16x32_bf16 v[62:65], v[156:159], v[188:191], v[62:65]
	v_mfma_f32_16x16x32_bf16 v[58:61], v[164:167], v[188:191], v[58:61]
	v_mfma_f32_16x16x32_bf16 v[46:49], v[156:159], v[196:199], v[46:49]
	v_mfma_f32_16x16x32_bf16 v[42:45], v[164:167], v[196:199], v[42:45]
	v_mfma_f32_16x16x32_bf16 v[30:33], v[156:159], v[204:207], v[30:33]
	v_mfma_f32_16x16x32_bf16 v[26:29], v[164:167], v[204:207], v[26:29]
	v_mfma_f32_16x16x32_bf16 v[14:17], v[156:159], v[216:219], v[14:17]
	v_mfma_f32_16x16x32_bf16 v[6:9], v[164:167], v[216:219], v[6:9]
	v_mfma_f32_16x16x32_bf16 v[62:65], v[160:163], v[192:195], v[62:65]
	v_mfma_f32_16x16x32_bf16 v[58:61], v[168:171], v[192:195], v[58:61]
	v_mfma_f32_16x16x32_bf16 v[46:49], v[160:163], v[200:203], v[46:49]
	v_mfma_f32_16x16x32_bf16 v[42:45], v[168:171], v[200:203], v[42:45]
	v_mfma_f32_16x16x32_bf16 v[30:33], v[160:163], v[212:215], v[30:33]
	v_mfma_f32_16x16x32_bf16 v[26:29], v[168:171], v[212:215], v[26:29]
	v_mfma_f32_16x16x32_bf16 v[14:17], v[160:163], v[220:223], v[14:17]
	v_mfma_f32_16x16x32_bf16 v[6:9], v[168:171], v[220:223], v[6:9]
	v_mfma_f32_16x16x32_bf16 v[54:57], v[172:175], v[188:191], v[54:57]
	v_mfma_f32_16x16x32_bf16 v[50:53], v[180:183], v[188:191], v[50:53]
	v_mfma_f32_16x16x32_bf16 v[38:41], v[172:175], v[196:199], v[38:41]
	v_mfma_f32_16x16x32_bf16 v[34:37], v[180:183], v[196:199], v[34:37]
	v_mfma_f32_16x16x32_bf16 v[22:25], v[172:175], v[204:207], v[22:25]
	v_mfma_f32_16x16x32_bf16 v[18:21], v[180:183], v[204:207], v[18:21]
	v_mfma_f32_16x16x32_bf16 v[10:13], v[172:175], v[216:219], v[10:13]
	v_mfma_f32_16x16x32_bf16 v[2:5], v[180:183], v[216:219], v[2:5]
	v_mfma_f32_16x16x32_bf16 v[54:57], v[176:179], v[192:195], v[54:57]
	v_mfma_f32_16x16x32_bf16 v[50:53], v[184:187], v[192:195], v[50:53]
	v_mfma_f32_16x16x32_bf16 v[38:41], v[176:179], v[200:203], v[38:41]
	v_mfma_f32_16x16x32_bf16 v[34:37], v[184:187], v[200:203], v[34:37]
	v_mfma_f32_16x16x32_bf16 v[22:25], v[176:179], v[212:215], v[22:25]
	v_mfma_f32_16x16x32_bf16 v[18:21], v[184:187], v[212:215], v[18:21]
	v_mfma_f32_16x16x32_bf16 v[10:13], v[176:179], v[220:223], v[10:13]
	v_mfma_f32_16x16x32_bf16 v[2:5], v[184:187], v[220:223], v[2:5]
	s_setprio 0
	s_barrier
	s_add_u32 s30, s30, 0x100
	s_addc_u32 s31, s31, 0
	s_add_u32 s58, s58, 0x100
	s_addc_u32 s59, s59, 0
	s_cmp_ge_i32 s61, s47
	s_cselect_b32 s99, 0, 1
	s_mov_b32 s34, s61
	s_cbranch_scc0 .LBB0_1171

; #define PG8_STAGE(bufoff, gbase, voff) do { _Pragma("unroll") for (int _i = 0; _i < 2; ++_i) \
;         __builtin_amdgcn_global_load_lds((const unsigned*)((const char*)(gbase) + (voff)[_i]), (PG8_LAS unsigned*)(lds + (bufoff) + ldsw + _i * 8192), 16, 0, 0); } while (0)
; #define PG8_LDA(dst, b, h) do { _Pragma("unroll") for (int m = 0; m < 4; ++m) { const bf16x8 f0_ = *(const PG8_LAS bf16x8*)(lds + PG8_SA(b, h) + aoff + m * 2048), f1_ = *(const PG8_LAS bf16x8*)(lds + PG8_SA(b, h) + aoff + m * 2048 + 1024); dst[m].set(f0_, f1_); } } while (0)
; #define PG8_LDB(dst, b, h) do { _Pragma("unroll") for (int n = 0; n < 2; ++n) { const bf16x8 f0_ = *(const PG8_LAS bf16x8*)(lds + PG8_SB(b, h) + boff + n * 2048), f1_ = *(const PG8_LAS bf16x8*)(lds + PG8_SB(b, h) + boff + n * 2048 + 1024); dst[n].set(f0_, f1_); } } while (0)
; #define PG8_WAIT_V(n) asm volatile("s_waitcnt vmcnt(" #n ")" ::: "memory")
; #define PG8_WAIT_L(n) asm volatile("s_waitcnt lgkmcnt(" #n ")" ::: "memory")
; #define PG8_BAR __builtin_amdgcn_s_barrier()
; #define PG8_SCHED __builtin_amdgcn_sched_barrier(0)
; template <class Epi, class Sched, bool ALIGN_EPI = false, bool SP2 = false>
; __device__ __forceinline__ void gemm_phase(PG8_LAS unsigned char* lds, const Gemm g, const Sched& S, const Epi& E) {
;     ...
;             PG8_LDB(B0, 0, 0); PG8_LDB(B1, 0, 1); PG8_SCHED; PG8_LDA(At, 0, 0); PG8_STAGE(PG8_SA(1, 1), a1 + hstep, voffA);
;             PG8_WAIT_V(8); PG8_WAIT_L(0); PG8_BAR; PG8_MMA(0, 0, At, B0); PG8_MMA(0, 1, At, B1); PG8_BAR; PG8_SCHED;
;             PG8_LDA(At, 0, 1); PG8_STAGE(PG8_SB(0, 0), b2, voffB); PG8_STAGE(PG8_SB(0, 1), b2 + hstepB, voffB); PG8_STAGE(PG8_SA(0, 0), a2, voffA);
;             PG8_WAIT_V(8); PG8_WAIT_L(0); PG8_BAR; PG8_MMA(1, 0, At, B0); PG8_MMA(1, 1, At, B1); PG8_BAR; PG8_SCHED;
.Lkr4_a:
	v_lshl_add_u64 v[148:149], s[30:31], 0, v[140:141]
	s_add_i32 m0, s40, 0xc000
	ds_read_b128 v[188:191], v154
	ds_read_b128 v[192:195], v154 offset:1024
	ds_read_b128 v[196:199], v154 offset:2048
	ds_read_b128 v[200:203], v154 offset:3072
	ds_read_b128 v[204:207], v154 offset:4096
	ds_read_b128 v[212:215], v154 offset:5120
	ds_read_b128 v[216:219], v154 offset:6144
	ds_read_b128 v[220:223], v154 offset:7168
	global_load_lds_dwordx4 v[148:149], off
	v_lshl_add_u64 v[148:149], s[30:31], 0, v[142:143]
	s_add_i32 m0, s40, 0xe000
	s_nop 0
	global_load_lds_dwordx4 v[148:149], off
	s_waitcnt vmcnt(8)
	s_waitcnt lgkmcnt(0)
	s_setprio 1
	s_barrier
	v_mfma_f32_16x16x32_bf16 v[126:129], v[156:159], v[188:191], v[126:129]
	v_mfma_f32_16x16x32_bf16 v[122:125], v[164:167], v[188:191], v[122:125]
	v_mfma_f32_16x16x32_bf16 v[110:113], v[156:159], v[196:199], v[110:113]
	v_mfma_f32_16x16x32_bf16 v[106:109], v[164:167], v[196:199], v[106:109]
	v_mfma_f32_16x16x32_bf16 v[94:97], v[156:159], v[204:207], v[94:97]
	v_mfma_f32_16x16x32_bf16 v[90:93], v[164:167], v[204:207], v[90:93]
	v_mfma_f32_16x16x32_bf16 v[78:81], v[156:159], v[216:219], v[78:81]
	v_mfma_f32_16x16x32_bf16 v[74:77], v[164:167], v[216:219], v[74:77]
	v_mfma_f32_16x16x32_bf16 v[126:129], v[160:163], v[192:195], v[126:129]
	v_mfma_f32_16x16x32_bf16 v[122:125], v[168:171], v[192:195], v[122:125]
	v_mfma_f32_16x16x32_bf16 v[110:113], v[160:163], v[200:203], v[110:113]
	v_mfma_f32_16x16x32_bf16 v[106:109], v[168:171], v[200:203], v[106:109]
	v_mfma_f32_16x16x32_bf16 v[94:97], v[160:163], v[212:215], v[94:97]
	v_mfma_f32_16x16x32_bf16 v[90:93], v[168:171], v[212:215], v[90:93]
	v_mfma_f32_16x16x32_bf16 v[78:81], v[160:163], v[220:223], v[78:81]
	v_mfma_f32_16x16x32_bf16 v[74:77], v[168:171], v[220:223], v[74:77]
	v_mfma_f32_16x16x32_bf16 v[118:121], v[172:175], v[188:191], v[118:121]
	v_mfma_f32_16x16x32_bf16 v[114:117], v[180:183], v[188:191], v[114:117]
	v_mfma_f32_16x16x32_bf16 v[102:105], v[172:175], v[196:199], v[102:105]
	v_mfma_f32_16x16x32_bf16 v[98:101], v[180:183], v[196:199], v[98:101]
	v_mfma_f32_16x16x32_bf16 v[86:89], v[172:175], v[204:207], v[86:89]
	v_mfma_f32_16x16x32_bf16 v[82:85], v[180:183], v[204:207], v[82:85]
	v_mfma_f32_16x16x32_bf16 v[70:73], v[172:175], v[216:219], v[70:73]
	v_mfma_f32_16x16x32_bf16 v[66:69], v[180:183], v[216:219], v[66:69]
	v_mfma_f32_16x16x32_bf16 v[118:121], v[176:179], v[192:195], v[118:121]
	v_mfma_f32_16x16x32_bf16 v[114:117], v[184:187], v[192:195], v[114:117]
	v_mfma_f32_16x16x32_bf16 v[102:105], v[176:179], v[200:203], v[102:105]
	v_mfma_f32_16x16x32_bf16 v[98:101], v[184:187], v[200:203], v[98:101]
	v_mfma_f32_16x16x32_bf16 v[86:89], v[176:179], v[212:215], v[86:89]
	v_mfma_f32_16x16x32_bf16 v[82:85], v[184:187], v[212:215], v[82:85]
	v_mfma_f32_16x16x32_bf16 v[70:73], v[176:179], v[220:223], v[70:73]
	v_mfma_f32_16x16x32_bf16 v[66:69], v[184:187], v[220:223], v[66:69]
	s_setprio 0
	s_barrier
	s_add_i32 s33, s52, s39
	v_lshl_add_u64 v[148:149], s[0:1], 0, v[132:133]
	s_mov_b32 m0, s33
	ds_read_b128 v[188:191], v154 offset:16384
	ds_read_b128 v[192:195], v154 offset:17408
	ds_read_b128 v[196:199], v154 offset:18432
	ds_read_b128 v[200:203], v154 offset:19456
	ds_read_b128 v[204:207], v154 offset:20480
	ds_read_b128 v[212:215], v154 offset:21504
	ds_read_b128 v[216:219], v154 offset:22528
	ds_read_b128 v[220:223], v154 offset:23552
	global_load_lds_dwordx4 v[148:149], off
	s_add_i32 m0, s33, 0x2000
	v_lshl_add_u64 v[208:209], s[0:1], 0, v[136:137]
	s_add_u32 s0, s0, s14
	s_addc_u32 s1, s1, s15
	s_add_i32 s33, s53, s39
	global_load_lds_dwordx4 v[208:209], off
	v_lshl_add_u64 v[224:225], s[0:1], 0, v[132:133]
	s_mov_b32 m0, s33
	v_lshl_add_u64 v[226:227], s[0:1], 0, v[136:137]
	global_load_lds_dwordx4 v[224:225], off
	s_add_i32 m0, s33, 0x2000
	v_lshl_add_u64 v[228:229], s[34:35], 0, v[130:131]
	global_load_lds_dwordx4 v[226:227], off
	v_lshl_add_u64 v[230:231], s[34:35], 0, v[134:135]
	s_waitcnt vmcnt(6)
	s_waitcnt lgkmcnt(0)
	s_setprio 1
	s_barrier
	v_mfma_f32_16x16x32_bf16 v[62:65], v[156:159], v[188:191], v[62:65]
	v_mfma_f32_16x16x32_bf16 v[58:61], v[164:167], v[188:191], v[58:61]
	v_mfma_f32_16x16x32_bf16 v[46:49], v[156:159], v[196:199], v[46:49]
	v_mfma_f32_16x16x32_bf16 v[42:45], v[164:167], v[196:199], v[42:45]
	v_mfma_f32_16x16x32_bf16 v[30:33], v[156:159], v[204:207], v[30:33]
	v_mfma_f32_16x16x32_bf16 v[26:29], v[164:167], v[204:207], v[26:29]
	v_mfma_f32_16x16x32_bf16 v[14:17], v[156:159], v[216:219], v[14:17]
	v_mfma_f32_16x16x32_bf16 v[6:9], v[164:167], v[216:219], v[6:9]
	v_mfma_f32_16x16x32_bf16 v[62:65], v[160:163], v[192:195], v[62:65]
	v_mfma_f32_16x16x32_bf16 v[58:61], v[168:171], v[192:195], v[58:61]
	v_mfma_f32_16x16x32_bf16 v[46:49], v[160:163], v[200:203], v[46:49]
	v_mfma_f32_16x16x32_bf16 v[42:45], v[168:171], v[200:203], v[42:45]
	v_mfma_f32_16x16x32_bf16 v[30:33], v[160:163], v[212:215], v[30:33]
	v_mfma_f32_16x16x32_bf16 v[26:29], v[168:171], v[212:215], v[26:29]
	v_mfma_f32_16x16x32_bf16 v[14:17], v[160:163], v[220:223], v[14:17]
	v_mfma_f32_16x16x32_bf16 v[6:9], v[168:171], v[220:223], v[6:9]
	v_mfma_f32_16x16x32_bf16 v[54:57], v[172:175], v[188:191], v[54:57]
	v_mfma_f32_16x16x32_bf16 v[50:53], v[180:183], v[188:191], v[50:53]
	v_mfma_f32_16x16x32_bf16 v[38:41], v[172:175], v[196:199], v[38:41]
	v_mfma_f32_16x16x32_bf16 v[34:37], v[180:183], v[196:199], v[34:37]
	v_mfma_f32_16x16x32_bf16 v[22:25], v[172:175], v[204:207], v[22:25]
	v_mfma_f32_16x16x32_bf16 v[18:21], v[180:183], v[204:207], v[18:21]
	v_mfma_f32_16x16x32_bf16 v[10:13], v[172:175], v[216:219], v[10:13]
	v_mfma_f32_16x16x32_bf16 v[2:5], v[180:183], v[216:219], v[2:5]
	v_mfma_f32_16x16x32_bf16 v[54:57], v[176:179], v[192:195], v[54:57]
	v_mfma_f32_16x16x32_bf16 v[50:53], v[184:187], v[192:195], v[50:53]
	v_mfma_f32_16x16x32_bf16 v[38:41], v[176:179], v[200:203], v[38:41]
	v_mfma_f32_16x16x32_bf16 v[34:37], v[184:187], v[200:203], v[34:37]
	v_mfma_f32_16x16x32_bf16 v[22:25], v[176:179], v[212:215], v[22:25]
	v_mfma_f32_16x16x32_bf16 v[18:21], v[184:187], v[212:215], v[18:21]
	v_mfma_f32_16x16x32_bf16 v[10:13], v[176:179], v[220:223], v[10:13]
	v_mfma_f32_16x16x32_bf16 v[2:5], v[184:187], v[220:223], v[2:5]
	s_setprio 0
	s_barrier
; #define PG8_STAGE(bufoff, gbase, voff) do { _Pragma("unroll") for (int _i = 0; _i < 2; ++_i) \
;         __builtin_amdgcn_global_load_lds((const unsigned*)((const char*)(gbase) + (voff)[_i]), (PG8_LAS unsigned*)(lds + (bufoff) + ldsw + _i * 8192), 16, 0, 0); } while (0)
; #define PG8_LDA(dst, b, h) do { _Pragma("unroll") for (int m = 0; m < 4; ++m) { const bf16x8 f0_ = *(const PG8_LAS bf16x8*)(lds + PG8_SA(b, h) + aoff + m * 2048), f1_ = *(const PG8_LAS bf16x8*)(lds + PG8_SA(b, h) + aoff + m * 2048 + 1024); dst[m].set(f0_, f1_); } } while (0)
; #define PG8_LDB(dst, b, h) do { _Pragma("unroll") for (int n = 0; n < 2; ++n) { const bf16x8 f0_ = *(const PG8_LAS bf16x8*)(lds + PG8_SB(b, h) + boff + n * 2048), f1_ = *(const PG8_LAS bf16x8*)(lds + PG8_SB(b, h) + boff + n * 2048 + 1024); dst[n].set(f0_, f1_); } } while (0)
; #define PG8_WAIT_V(n) asm volatile("s_waitcnt vmcnt(" #n ")" ::: "memory")
; #define PG8_WAIT_L(n) asm volatile("s_waitcnt lgkmcnt(" #n ")" ::: "memory")
; #define PG8_BAR __builtin_amdgcn_s_barrier()
; #define PG8_SCHED __builtin_amdgcn_sched_barrier(0)
; template <class Epi, class Sched, bool ALIGN_EPI = false, bool SP2 = false>
; __device__ __forceinline__ void gemm_phase(PG8_LAS unsigned char* lds, const Gemm g, const Sched& S, const Epi& E) {
;     ...
;             PG8_LDB(B0, 1, 0); PG8_LDB(B1, 1, 1); PG8_SCHED; PG8_LDA(At, 1, 0); PG8_STAGE(PG8_SA(0, 1), a2 + hstep, voffA);
;             PG8_WAIT_V(8); PG8_WAIT_L(0); PG8_BAR; PG8_MMA(0, 0, At, B0); PG8_MMA(0, 1, At, B1); PG8_BAR; PG8_SCHED;
;             PG8_LDA(At, 1, 1); PG8_STAGE(PG8_SB(1, 0), b3, voffB); PG8_STAGE(PG8_SB(1, 1), b3 + hstepB, voffB); PG8_STAGE(PG8_SA(1, 0), a3, voffA);
	s_add_i32 s33, 0, 0x18000
	s_add_i32 s63, 0, 0x1c000
	v_add_u32_e32 v168, s33, v1
	v_add_u32_e32 v184, s63, v1
	ds_read_b128 v[156:159], v168
	ds_read_b128 v[160:163], v168 offset:1024
	ds_read_b128 v[164:167], v168 offset:2048
	ds_read_b128 v[168:171], v168 offset:3072
	ds_read_b128 v[172:175], v184
	ds_read_b128 v[176:179], v184 offset:1024
	ds_read_b128 v[180:183], v184 offset:2048
	ds_read_b128 v[184:187], v184 offset:3072
	s_add_u32 s0, s34, s12
	s_addc_u32 s1, s35, s13
	s_mov_b32 m0, s42
	v_lshl_add_u64 v[232:233], s[0:1], 0, v[130:131]
	ds_read_b128 v[188:191], v154 offset:32768
	ds_read_b128 v[192:195], v154 offset:33792
	ds_read_b128 v[196:199], v154 offset:34816
	ds_read_b128 v[200:203], v154 offset:35840
	ds_read_b128 v[204:207], v154 offset:36864
	ds_read_b128 v[212:215], v154 offset:37888
	ds_read_b128 v[216:219], v154 offset:38912
	ds_read_b128 v[220:223], v154 offset:39936
	s_mov_b32 m0, s40
	s_nop 0
	global_load_lds_dwordx4 v[228:229], off
	s_mov_b32 m0, s41
	s_nop 0
	global_load_lds_dwordx4 v[230:231], off
	s_mov_b32 m0, s42
	s_nop 0
	global_load_lds_dwordx4 v[232:233], off
	v_lshl_add_u64 v[232:233], s[0:1], 0, v[134:135]
	s_mov_b32 m0, s43
	s_nop 0
	global_load_lds_dwordx4 v[232:233], off
	s_waitcnt vmcnt(8)
	s_waitcnt lgkmcnt(0)
	s_setprio 1
	s_barrier
	v_mfma_f32_16x16x32_bf16 v[126:129], v[156:159], v[188:191], v[126:129]
	v_mfma_f32_16x16x32_bf16 v[122:125], v[164:167], v[188:191], v[122:125]
	v_mfma_f32_16x16x32_bf16 v[110:113], v[156:159], v[196:199], v[110:113]
	v_mfma_f32_16x16x32_bf16 v[106:109], v[164:167], v[196:199], v[106:109]
	v_mfma_f32_16x16x32_bf16 v[94:97], v[156:159], v[204:207], v[94:97]
	v_mfma_f32_16x16x32_bf16 v[90:93], v[164:167], v[204:207], v[90:93]
	v_mfma_f32_16x16x32_bf16 v[78:81], v[156:159], v[216:219], v[78:81]
	v_mfma_f32_16x16x32_bf16 v[74:77], v[164:167], v[216:219], v[74:77]
	v_mfma_f32_16x16x32_bf16 v[126:129], v[160:163], v[192:195], v[126:129]
	v_mfma_f32_16x16x32_bf16 v[122:125], v[168:171], v[192:195], v[122:125]
	v_mfma_f32_16x16x32_bf16 v[110:113], v[160:163], v[200:203], v[110:113]
	v_mfma_f32_16x16x32_bf16 v[106:109], v[168:171], v[200:203], v[106:109]
	v_mfma_f32_16x16x32_bf16 v[94:97], v[160:163], v[212:215], v[94:97]
	v_mfma_f32_16x16x32_bf16 v[90:93], v[168:171], v[212:215], v[90:93]
	v_mfma_f32_16x16x32_bf16 v[78:81], v[160:163], v[220:223], v[78:81]
	v_mfma_f32_16x16x32_bf16 v[74:77], v[168:171], v[220:223], v[74:77]
	v_mfma_f32_16x16x32_bf16 v[118:121], v[172:175], v[188:191], v[118:121]
	v_mfma_f32_16x16x32_bf16 v[114:117], v[180:183], v[188:191], v[114:117]
	v_mfma_f32_16x16x32_bf16 v[102:105], v[172:175], v[196:199], v[102:105]
	v_mfma_f32_16x16x32_bf16 v[98:101], v[180:183], v[196:199], v[98:101]
	v_mfma_f32_16x16x32_bf16 v[86:89], v[172:175], v[204:207], v[86:89]
	v_mfma_f32_16x16x32_bf16 v[82:85], v[180:183], v[204:207], v[82:85]
	v_mfma_f32_16x16x32_bf16 v[70:73], v[172:175], v[216:219], v[70:73]
	v_mfma_f32_16x16x32_bf16 v[66:69], v[180:183], v[216:219], v[66:69]
	v_mfma_f32_16x16x32_bf16 v[118:121], v[176:179], v[192:195], v[118:121]
	v_mfma_f32_16x16x32_bf16 v[114:117], v[184:187], v[192:195], v[114:117]
	v_mfma_f32_16x16x32_bf16 v[102:105], v[176:179], v[200:203], v[102:105]
	v_mfma_f32_16x16x32_bf16 v[98:101], v[184:187], v[200:203], v[98:101]
	v_mfma_f32_16x16x32_bf16 v[86:89], v[176:179], v[212:215], v[86:89]
	v_mfma_f32_16x16x32_bf16 v[82:85], v[184:187], v[212:215], v[82:85]
	v_mfma_f32_16x16x32_bf16 v[70:73], v[176:179], v[220:223], v[70:73]
	v_mfma_f32_16x16x32_bf16 v[66:69], v[184:187], v[220:223], v[66:69]
	s_setprio 0
	s_barrier
	s_add_i32 s0, s33, s39
	v_lshl_add_u64 v[148:149], v[148:149], 0, s[22:23]
	s_mov_b32 m0, s0
	ds_read_b128 v[188:191], v154 offset:49152
	ds_read_b128 v[192:195], v154 offset:50176
	ds_read_b128 v[196:199], v154 offset:51200
	ds_read_b128 v[200:203], v154 offset:52224
	ds_read_b128 v[204:207], v154 offset:53248
	ds_read_b128 v[212:215], v154 offset:54272
	ds_read_b128 v[216:219], v154 offset:55296
	ds_read_b128 v[220:223], v154 offset:56320
	global_load_lds_dwordx4 v[148:149], off
	v_lshl_add_u64 v[148:149], v[208:209], 0, s[22:23]
	s_add_i32 m0, s0, 0x2000
	s_add_i32 s0, s63, s39
	global_load_lds_dwordx4 v[148:149], off
	v_lshl_add_u64 v[148:149], v[224:225], 0, s[22:23]
	s_mov_b32 m0, s0
	s_nop 0
	global_load_lds_dwordx4 v[148:149], off
	v_lshl_add_u64 v[148:149], v[226:227], 0, s[22:23]
	s_add_i32 m0, s0, 0x2000
	s_nop 0
	global_load_lds_dwordx4 v[148:149], off
	s_cmp_ge_i32 s61, s48
	s_cbranch_scc0 .Lkr4_b
	v_lshl_add_u64 v[148:149], v[228:229], 0, s[22:23]
	s_mov_b32 m0, s46
	s_nop 0
	global_load_lds_dwordx4 v[148:149], off
	v_lshl_add_u64 v[148:149], v[230:231], 0, s[22:23]
	s_mov_b32 m0, s47
	s_nop 0
	global_load_lds_dwordx4 v[148:149], off
; #define PG8_WAIT_V(n) asm volatile("s_waitcnt vmcnt(" #n ")" ::: "memory")
; #define PG8_WAIT_L(n) asm volatile("s_waitcnt lgkmcnt(" #n ")" ::: "memory")
; #define PG8_BAR __builtin_amdgcn_s_barrier()
; #define PG8_SCHED __builtin_amdgcn_sched_barrier(0)
; template <class Epi, class Sched, bool ALIGN_EPI = false, bool SP2 = false>
; __device__ __forceinline__ void gemm_phase(PG8_LAS unsigned char* lds, const Gemm g, const Sched& S, const Epi& E) {
;     ...
;         for (int t = 0; t < nt; t += 2) {
;             if constexpr (Epi::MIDK) { if (t == (nt >> 1)) E.mid(acc, cur, wr, wc, fr, fq); }
;             const bool last = (t == nt - 2);
;             const char* a1 = cA + (size_t)(t + 1) * kstep;
;             const char* a2 = last ? nA : cA + (size_t)(t + 2) * kstep; const char* b2 = last ? nB : cB + (size_t)(t + 2) * kstep;
;             const char* a3 = a2 + kstep; const char* b3 = b2 + kstep;
;     ...
;             PG8_WAIT_V(8); PG8_WAIT_L(0); PG8_BAR; PG8_MMA(1, 0, At, B0); PG8_MMA(1, 1, At, B1); PG8_BAR; PG8_SCHED;
.Lkr4_b:
	s_waitcnt vmcnt(6)
	s_waitcnt lgkmcnt(0)
	s_setprio 1
	s_barrier
	v_mfma_f32_16x16x32_bf16 v[62:65], v[156:159], v[188:191], v[62:65]
	v_mfma_f32_16x16x32_bf16 v[58:61], v[164:167], v[188:191], v[58:61]
	v_mfma_f32_16x16x32_bf16 v[46:49], v[156:159], v[196:199], v[46:49]
	v_mfma_f32_16x16x32_bf16 v[42:45], v[164:167], v[196:199], v[42:45]
	v_mfma_f32_16x16x32_bf16 v[30:33], v[156:159], v[204:207], v[30:33]
	v_mfma_f32_16x16x32_bf16 v[26:29], v[164:167], v[204:207], v[26:29]
	v_mfma_f32_16x16x32_bf16 v[14:17], v[156:159], v[216:219], v[14:17]
	v_mfma_f32_16x16x32_bf16 v[6:9], v[164:167], v[216:219], v[6:9]
	v_mfma_f32_16x16x32_bf16 v[62:65], v[160:163], v[192:195], v[62:65]
	v_mfma_f32_16x16x32_bf16 v[58:61], v[168:171], v[192:195], v[58:61]
	v_mfma_f32_16x16x32_bf16 v[46:49], v[160:163], v[200:203], v[46:49]
	v_mfma_f32_16x16x32_bf16 v[42:45], v[168:171], v[200:203], v[42:45]
	v_mfma_f32_16x16x32_bf16 v[30:33], v[160:163], v[212:215], v[30:33]
	v_mfma_f32_16x16x32_bf16 v[26:29], v[168:171], v[212:215], v[26:29]
	v_mfma_f32_16x16x32_bf16 v[14:17], v[160:163], v[220:223], v[14:17]
	v_mfma_f32_16x16x32_bf16 v[6:9], v[168:171], v[220:223], v[6:9]
	v_mfma_f32_16x16x32_bf16 v[54:57], v[172:175], v[188:191], v[54:57]
	v_mfma_f32_16x16x32_bf16 v[50:53], v[180:183], v[188:191], v[50:53]
	v_mfma_f32_16x16x32_bf16 v[38:41], v[172:175], v[196:199], v[38:41]
	v_mfma_f32_16x16x32_bf16 v[34:37], v[180:183], v[196:199], v[34:37]
	v_mfma_f32_16x16x32_bf16 v[22:25], v[172:175], v[204:207], v[22:25]
	v_mfma_f32_16x16x32_bf16 v[18:21], v[180:183], v[204:207], v[18:21]
	v_mfma_f32_16x16x32_bf16 v[10:13], v[172:175], v[216:219], v[10:13]
	v_mfma_f32_16x16x32_bf16 v[2:5], v[180:183], v[216:219], v[2:5]
	v_mfma_f32_16x16x32_bf16 v[54:57], v[176:179], v[192:195], v[54:57]
	v_mfma_f32_16x16x32_bf16 v[50:53], v[184:187], v[192:195], v[50:53]
	v_mfma_f32_16x16x32_bf16 v[38:41], v[176:179], v[200:203], v[38:41]
	v_mfma_f32_16x16x32_bf16 v[34:37], v[184:187], v[200:203], v[34:37]
	v_mfma_f32_16x16x32_bf16 v[22:25], v[176:179], v[212:215], v[22:25]
	v_mfma_f32_16x16x32_bf16 v[18:21], v[184:187], v[212:215], v[18:21]
	v_mfma_f32_16x16x32_bf16 v[10:13], v[176:179], v[220:223], v[10:13]
	v_mfma_f32_16x16x32_bf16 v[2:5], v[184:187], v[220:223], v[2:5]
	s_setprio 0
	s_barrier
	s_add_u32 s30, s30, 0x100
	s_addc_u32 s31, s31, 0
	s_add_u32 s58, s58, 0x100
	s_addc_u32 s59, s59, 0
	s_cmp_ge_i32 s61, s48
	s_cselect_b32 s99, 0, 1
	s_mov_b32 s34, s61
	s_cbranch_scc0 .LBB0_1592

; #define PG8_STAGE(bufoff, gbase, voff) do { _Pragma("unroll") for (int _i = 0; _i < 2; ++_i) \
;         __builtin_amdgcn_global_load_lds((const unsigned*)((const char*)(gbase) + (voff)[_i]), (PG8_LAS unsigned*)(lds + (bufoff) + ldsw + _i * 8192), 16, 0, 0); } while (0)
; #define PG8_LDA(dst, b, h) do { _Pragma("unroll") for (int m = 0; m < 4; ++m) { const bf16x8 f0_ = *(const PG8_LAS bf16x8*)(lds + PG8_SA(b, h) + aoff + m * 2048), f1_ = *(const PG8_LAS bf16x8*)(lds + PG8_SA(b, h) + aoff + m * 2048 + 1024); dst[m].set(f0_, f1_); } } while (0)
; #define PG8_LDB(dst, b, h) do { _Pragma("unroll") for (int n = 0; n < 2; ++n) { const bf16x8 f0_ = *(const PG8_LAS bf16x8*)(lds + PG8_SB(b, h) + boff + n * 2048), f1_ = *(const PG8_LAS bf16x8*)(lds + PG8_SB(b, h) + boff + n * 2048 + 1024); dst[n].set(f0_, f1_); } } while (0)
; #define PG8_WAIT_V(n) asm volatile("s_waitcnt vmcnt(" #n ")" ::: "memory")
; #define PG8_WAIT_L(n) asm volatile("s_waitcnt lgkmcnt(" #n ")" ::: "memory")
; #define PG8_BAR __builtin_amdgcn_s_barrier()
; #define PG8_SCHED __builtin_amdgcn_sched_barrier(0)
; template <class Epi, class Sched, bool ALIGN_EPI = false, bool SP2 = false>
; __device__ __forceinline__ void gemm_phase(PG8_LAS unsigned char* lds, const Gemm g, const Sched& S, const Epi& E) {
;     ...
;             PG8_LDB(B0, 0, 0); PG8_LDB(B1, 0, 1); PG8_SCHED; PG8_LDA(At, 0, 0); PG8_STAGE(PG8_SA(1, 1), a1 + hstep, voffA);
;             PG8_WAIT_V(8); PG8_WAIT_L(0); PG8_BAR; PG8_MMA(0, 0, At, B0); PG8_MMA(0, 1, At, B1); PG8_BAR; PG8_SCHED;
;             PG8_LDA(At, 0, 1); PG8_STAGE(PG8_SB(0, 0), b2, voffB); PG8_STAGE(PG8_SB(0, 1), b2 + hstepB, voffB); PG8_STAGE(PG8_SA(0, 0), a2, voffA);
;             PG8_WAIT_V(8); PG8_WAIT_L(0); PG8_BAR; PG8_MMA(1, 0, At, B0); PG8_MMA(1, 1, At, B1); PG8_BAR; PG8_SCHED;
.Lkr5_a:
	v_lshl_add_u64 v[192:193], s[46:47], 0, v[176:177]
	s_add_i32 m0, s10, 0xc000
	ds_read_b128 v[184:187], v199
	ds_read_b128 v[188:191], v199 offset:1024
	ds_read_b128 v[212:215], v199 offset:2048
	ds_read_b128 v[216:219], v199 offset:3072
	ds_read_b128 v[220:223], v199 offset:4096
	ds_read_b128 v[224:227], v199 offset:5120
	ds_read_b128 v[228:231], v199 offset:6144
	ds_read_b128 v[232:235], v199 offset:7168
	global_load_lds_dwordx4 v[192:193], off
	v_lshl_add_u64 v[192:193], s[46:47], 0, v[178:179]
	s_add_i32 m0, s10, 0xe000
	s_nop 0
	global_load_lds_dwordx4 v[192:193], off
	s_waitcnt vmcnt(8)
	s_waitcnt lgkmcnt(0)
	s_setprio 1
	s_barrier
	v_mfma_scale_f32_16x16x128_f8f6f4 v[158:161], v[18:25], v[184:191], v[158:161], v200, v201 op_sel_hi:[0,0,0]
	v_mfma_scale_f32_16x16x128_f8f6f4 v[154:157], v[26:33], v[184:191], v[154:157], v200, v201 op_sel_hi:[0,0,0]
	v_mfma_scale_f32_16x16x128_f8f6f4 v[142:145], v[18:25], v[212:219], v[142:145], v200, v201 op_sel_hi:[0,0,0]
	v_mfma_scale_f32_16x16x128_f8f6f4 v[138:141], v[26:33], v[212:219], v[138:141], v200, v201 op_sel_hi:[0,0,0]
	v_mfma_scale_f32_16x16x128_f8f6f4 v[126:129], v[18:25], v[220:227], v[126:129], v200, v201 op_sel_hi:[0,0,0]
	v_mfma_scale_f32_16x16x128_f8f6f4 v[122:125], v[26:33], v[220:227], v[122:125], v200, v201 op_sel_hi:[0,0,0]
	v_mfma_scale_f32_16x16x128_f8f6f4 v[110:113], v[18:25], v[228:235], v[110:113], v200, v201 op_sel_hi:[0,0,0]
	v_mfma_scale_f32_16x16x128_f8f6f4 v[106:109], v[26:33], v[228:235], v[106:109], v200, v201 op_sel_hi:[0,0,0]
	v_mfma_scale_f32_16x16x128_f8f6f4 v[150:153], v[2:9], v[184:191], v[150:153], v200, v201 op_sel_hi:[0,0,0]
	v_mfma_scale_f32_16x16x128_f8f6f4 v[146:149], v[10:17], v[184:191], v[146:149], v200, v201 op_sel_hi:[0,0,0]
	v_mfma_scale_f32_16x16x128_f8f6f4 v[134:137], v[2:9], v[212:219], v[134:137], v200, v201 op_sel_hi:[0,0,0]
	v_mfma_scale_f32_16x16x128_f8f6f4 v[130:133], v[10:17], v[212:219], v[130:133], v200, v201 op_sel_hi:[0,0,0]
	v_mfma_scale_f32_16x16x128_f8f6f4 v[118:121], v[2:9], v[220:227], v[118:121], v200, v201 op_sel_hi:[0,0,0]
	v_mfma_scale_f32_16x16x128_f8f6f4 v[114:117], v[10:17], v[220:227], v[114:117], v200, v201 op_sel_hi:[0,0,0]
	v_mfma_scale_f32_16x16x128_f8f6f4 v[102:105], v[2:9], v[228:235], v[102:105], v200, v201 op_sel_hi:[0,0,0]
	v_mfma_scale_f32_16x16x128_f8f6f4 v[98:101], v[10:17], v[228:235], v[98:101], v200, v201 op_sel_hi:[0,0,0]
	s_setprio 0
	s_barrier
	s_add_i32 s0, s73, s9
	v_lshl_add_u64 v[184:185], s[50:51], 0, v[164:165]
	s_mov_b32 m0, s0
	ds_read_b128 v[212:215], v199 offset:16384
	ds_read_b128 v[216:219], v199 offset:17408
	ds_read_b128 v[220:223], v199 offset:18432
	ds_read_b128 v[224:227], v199 offset:19456
	ds_read_b128 v[228:231], v199 offset:20480
	ds_read_b128 v[232:235], v199 offset:21504
	ds_read_b128 v[236:239], v199 offset:22528
	ds_read_b128 v[240:243], v199 offset:23552
	global_load_lds_dwordx4 v[184:185], off
	s_add_i32 m0, s0, 0x2000
	s_add_u32 s0, s50, s14
	v_lshl_add_u64 v[186:187], s[50:51], 0, v[168:169]
	s_addc_u32 s1, s51, s15
	s_add_i32 s33, s74, s9
	global_load_lds_dwordx4 v[186:187], off
	v_lshl_add_u64 v[188:189], s[0:1], 0, v[164:165]
	s_mov_b32 m0, s33
	v_lshl_add_u64 v[190:191], s[0:1], 0, v[168:169]
	global_load_lds_dwordx4 v[188:189], off
	s_add_i32 m0, s33, 0x2000
	v_lshl_add_u64 v[192:193], s[48:49], 0, v[162:163]
	global_load_lds_dwordx4 v[190:191], off
	v_lshl_add_u64 v[194:195], s[48:49], 0, v[166:167]
	s_waitcnt vmcnt(6)
	s_waitcnt lgkmcnt(0)
	s_setprio 1
	s_barrier
	v_mfma_scale_f32_16x16x128_f8f6f4 v[94:97], v[18:25], v[212:219], v[94:97], v200, v201 op_sel_hi:[0,0,0]
	v_mfma_scale_f32_16x16x128_f8f6f4 v[90:93], v[26:33], v[212:219], v[90:93], v200, v201 op_sel_hi:[0,0,0]
	v_mfma_scale_f32_16x16x128_f8f6f4 v[78:81], v[18:25], v[220:227], v[78:81], v200, v201 op_sel_hi:[0,0,0]
	v_mfma_scale_f32_16x16x128_f8f6f4 v[74:77], v[26:33], v[220:227], v[74:77], v200, v201 op_sel_hi:[0,0,0]
	v_mfma_scale_f32_16x16x128_f8f6f4 v[62:65], v[18:25], v[228:235], v[62:65], v200, v201 op_sel_hi:[0,0,0]
	v_mfma_scale_f32_16x16x128_f8f6f4 v[58:61], v[26:33], v[228:235], v[58:61], v200, v201 op_sel_hi:[0,0,0]
	v_mfma_scale_f32_16x16x128_f8f6f4 v[46:49], v[18:25], v[236:243], v[46:49], v200, v201 op_sel_hi:[0,0,0]
	v_mfma_scale_f32_16x16x128_f8f6f4 v[42:45], v[26:33], v[236:243], v[42:45], v200, v201 op_sel_hi:[0,0,0]
	v_mfma_scale_f32_16x16x128_f8f6f4 v[86:89], v[2:9], v[212:219], v[86:89], v200, v201 op_sel_hi:[0,0,0]
	v_mfma_scale_f32_16x16x128_f8f6f4 v[82:85], v[10:17], v[212:219], v[82:85], v200, v201 op_sel_hi:[0,0,0]
	v_mfma_scale_f32_16x16x128_f8f6f4 v[70:73], v[2:9], v[220:227], v[70:73], v200, v201 op_sel_hi:[0,0,0]
	v_mfma_scale_f32_16x16x128_f8f6f4 v[66:69], v[10:17], v[220:227], v[66:69], v200, v201 op_sel_hi:[0,0,0]
	v_mfma_scale_f32_16x16x128_f8f6f4 v[54:57], v[2:9], v[228:235], v[54:57], v200, v201 op_sel_hi:[0,0,0]
	v_mfma_scale_f32_16x16x128_f8f6f4 v[50:53], v[10:17], v[228:235], v[50:53], v200, v201 op_sel_hi:[0,0,0]
	v_mfma_scale_f32_16x16x128_f8f6f4 v[38:41], v[2:9], v[236:243], v[38:41], v200, v201 op_sel_hi:[0,0,0]
	v_mfma_scale_f32_16x16x128_f8f6f4 v[34:37], v[10:17], v[236:243], v[34:37], v200, v201 op_sel_hi:[0,0,0]
	s_setprio 0
	s_barrier
; #define PG8_STAGE(bufoff, gbase, voff) do { _Pragma("unroll") for (int _i = 0; _i < 2; ++_i) \
;         __builtin_amdgcn_global_load_lds((const unsigned*)((const char*)(gbase) + (voff)[_i]), (PG8_LAS unsigned*)(lds + (bufoff) + ldsw + _i * 8192), 16, 0, 0); } while (0)
; #define PG8_LDA(dst, b, h) do { _Pragma("unroll") for (int m = 0; m < 4; ++m) { const bf16x8 f0_ = *(const PG8_LAS bf16x8*)(lds + PG8_SA(b, h) + aoff + m * 2048), f1_ = *(const PG8_LAS bf16x8*)(lds + PG8_SA(b, h) + aoff + m * 2048 + 1024); dst[m].set(f0_, f1_); } } while (0)
; #define PG8_LDB(dst, b, h) do { _Pragma("unroll") for (int n = 0; n < 2; ++n) { const bf16x8 f0_ = *(const PG8_LAS bf16x8*)(lds + PG8_SB(b, h) + boff + n * 2048), f1_ = *(const PG8_LAS bf16x8*)(lds + PG8_SB(b, h) + boff + n * 2048 + 1024); dst[n].set(f0_, f1_); } } while (0)
; #define PG8_WAIT_V(n) asm volatile("s_waitcnt vmcnt(" #n ")" ::: "memory")
; #define PG8_WAIT_L(n) asm volatile("s_waitcnt lgkmcnt(" #n ")" ::: "memory")
; #define PG8_BAR __builtin_amdgcn_s_barrier()
; #define PG8_SCHED __builtin_amdgcn_sched_barrier(0)
; template <class Epi, class Sched, bool ALIGN_EPI = false, bool SP2 = false>
; __device__ __forceinline__ void gemm_phase(PG8_LAS unsigned char* lds, const Gemm g, const Sched& S, const Epi& E) {
;     ...
;             PG8_LDB(B0, 1, 0); PG8_LDB(B1, 1, 1); PG8_SCHED; PG8_LDA(At, 1, 0); PG8_STAGE(PG8_SA(0, 1), a2 + hstep, voffA);
;             PG8_WAIT_V(8); PG8_WAIT_L(0); PG8_BAR; PG8_MMA(0, 0, At, B0); PG8_MMA(0, 1, At, B1); PG8_BAR; PG8_SCHED;
;             PG8_LDA(At, 1, 1); PG8_STAGE(PG8_SB(1, 0), b3, voffB); PG8_STAGE(PG8_SB(1, 1), b3 + hstepB, voffB); PG8_STAGE(PG8_SA(1, 0), a3, voffA);
;             PG8_WAIT_V(8); PG8_WAIT_L(0); PG8_BAR; PG8_MMA(1, 0, At, B0); PG8_MMA(1, 1, At, B1); PG8_BAR; PG8_SCHED;
	s_add_i32 s33, 0, 0x18000
	s_add_i32 s50, 0, 0x1c000
	v_add_u32_e32 v14, s33, v173
	v_add_u32_e32 v30, s50, v173
	ds_read_b128 v[2:5], v14
	ds_read_b128 v[6:9], v14 offset:1024
	ds_read_b128 v[10:13], v14 offset:2048
	ds_read_b128 v[14:17], v14 offset:3072
	ds_read_b128 v[18:21], v30
	ds_read_b128 v[22:25], v30 offset:1024
	ds_read_b128 v[26:29], v30 offset:2048
	ds_read_b128 v[30:33], v30 offset:3072
	s_add_u32 s0, s48, s12
	s_addc_u32 s1, s49, s13
	s_mov_b32 m0, s52
	v_lshl_add_u64 v[204:205], s[0:1], 0, v[162:163]
	ds_read_b128 v[212:215], v199 offset:32768
	ds_read_b128 v[216:219], v199 offset:33792
	ds_read_b128 v[220:223], v199 offset:34816
	ds_read_b128 v[224:227], v199 offset:35840
	ds_read_b128 v[228:231], v199 offset:36864
	ds_read_b128 v[232:235], v199 offset:37888
	ds_read_b128 v[236:239], v199 offset:38912
	ds_read_b128 v[240:243], v199 offset:39936
	s_mov_b32 m0, s10
	s_nop 0
	global_load_lds_dwordx4 v[192:193], off
	s_mov_b32 m0, s11
	s_nop 0
	global_load_lds_dwordx4 v[194:195], off
	s_mov_b32 m0, s52
	s_nop 0
	global_load_lds_dwordx4 v[204:205], off
	v_lshl_add_u64 v[204:205], s[0:1], 0, v[166:167]
	s_mov_b32 m0, s53
	s_nop 0
	global_load_lds_dwordx4 v[204:205], off
	s_waitcnt vmcnt(8)
	s_waitcnt lgkmcnt(0)
	s_setprio 1
	s_barrier
	v_mfma_scale_f32_16x16x128_f8f6f4 v[158:161], v[2:9], v[212:219], v[158:161], v200, v201 op_sel_hi:[0,0,0]
	v_mfma_scale_f32_16x16x128_f8f6f4 v[154:157], v[10:17], v[212:219], v[154:157], v200, v201 op_sel_hi:[0,0,0]
	v_mfma_scale_f32_16x16x128_f8f6f4 v[142:145], v[2:9], v[220:227], v[142:145], v200, v201 op_sel_hi:[0,0,0]
	v_mfma_scale_f32_16x16x128_f8f6f4 v[138:141], v[10:17], v[220:227], v[138:141], v200, v201 op_sel_hi:[0,0,0]
	v_mfma_scale_f32_16x16x128_f8f6f4 v[126:129], v[2:9], v[228:235], v[126:129], v200, v201 op_sel_hi:[0,0,0]
	v_mfma_scale_f32_16x16x128_f8f6f4 v[122:125], v[10:17], v[228:235], v[122:125], v200, v201 op_sel_hi:[0,0,0]
	v_mfma_scale_f32_16x16x128_f8f6f4 v[110:113], v[2:9], v[236:243], v[110:113], v200, v201 op_sel_hi:[0,0,0]
	v_mfma_scale_f32_16x16x128_f8f6f4 v[106:109], v[10:17], v[236:243], v[106:109], v200, v201 op_sel_hi:[0,0,0]
	v_mfma_scale_f32_16x16x128_f8f6f4 v[150:153], v[18:25], v[212:219], v[150:153], v200, v201 op_sel_hi:[0,0,0]
	v_mfma_scale_f32_16x16x128_f8f6f4 v[146:149], v[26:33], v[212:219], v[146:149], v200, v201 op_sel_hi:[0,0,0]
	v_mfma_scale_f32_16x16x128_f8f6f4 v[134:137], v[18:25], v[220:227], v[134:137], v200, v201 op_sel_hi:[0,0,0]
	v_mfma_scale_f32_16x16x128_f8f6f4 v[130:133], v[26:33], v[220:227], v[130:133], v200, v201 op_sel_hi:[0,0,0]
	v_mfma_scale_f32_16x16x128_f8f6f4 v[118:121], v[18:25], v[228:235], v[118:121], v200, v201 op_sel_hi:[0,0,0]
	v_mfma_scale_f32_16x16x128_f8f6f4 v[114:117], v[26:33], v[228:235], v[114:117], v200, v201 op_sel_hi:[0,0,0]
	v_mfma_scale_f32_16x16x128_f8f6f4 v[102:105], v[18:25], v[236:243], v[102:105], v200, v201 op_sel_hi:[0,0,0]
	v_mfma_scale_f32_16x16x128_f8f6f4 v[98:101], v[26:33], v[236:243], v[98:101], v200, v201 op_sel_hi:[0,0,0]
	s_setprio 0
	s_barrier
	s_add_i32 s0, s33, s9
	v_lshl_add_u64 v[184:185], v[184:185], 0, s[28:29]
	s_mov_b32 m0, s0
	ds_read_b128 v[212:215], v199 offset:49152
	ds_read_b128 v[216:219], v199 offset:50176
	ds_read_b128 v[220:223], v199 offset:51200
	ds_read_b128 v[224:227], v199 offset:52224
	ds_read_b128 v[228:231], v199 offset:53248
	ds_read_b128 v[232:235], v199 offset:54272
	ds_read_b128 v[236:239], v199 offset:55296
	ds_read_b128 v[240:243], v199 offset:56320
	global_load_lds_dwordx4 v[184:185], off
	v_lshl_add_u64 v[184:185], v[186:187], 0, s[28:29]
	s_add_i32 m0, s0, 0x2000
	s_add_i32 s0, s50, s9
	global_load_lds_dwordx4 v[184:185], off
	v_lshl_add_u64 v[184:185], v[188:189], 0, s[28:29]
	s_mov_b32 m0, s0
	s_nop 0
	global_load_lds_dwordx4 v[184:185], off
	v_lshl_add_u64 v[184:185], v[190:191], 0, s[28:29]
	s_add_i32 m0, s0, 0x2000
	s_nop 0
	global_load_lds_dwordx4 v[184:185], off
	s_cmp_ge_i32 s82, s58
	s_cbranch_scc0 .Lkr5_b
	v_lshl_add_u64 v[184:185], v[192:193], 0, s[28:29]
	s_mov_b32 m0, s56
	s_nop 0
	global_load_lds_dwordx4 v[184:185], off
	v_lshl_add_u64 v[184:185], v[194:195], 0, s[28:29]
	s_mov_b32 m0, s57
	s_nop 0
	global_load_lds_dwordx4 v[184:185], off
.Lkr5_b:
	s_waitcnt vmcnt(6)
	s_waitcnt lgkmcnt(0)
	s_setprio 1
	s_barrier
	v_mfma_scale_f32_16x16x128_f8f6f4 v[94:97], v[2:9], v[212:219], v[94:97], v200, v201 op_sel_hi:[0,0,0]
	v_mfma_scale_f32_16x16x128_f8f6f4 v[90:93], v[10:17], v[212:219], v[90:93], v200, v201 op_sel_hi:[0,0,0]
	v_mfma_scale_f32_16x16x128_f8f6f4 v[78:81], v[2:9], v[220:227], v[78:81], v200, v201 op_sel_hi:[0,0,0]
	v_mfma_scale_f32_16x16x128_f8f6f4 v[74:77], v[10:17], v[220:227], v[74:77], v200, v201 op_sel_hi:[0,0,0]
	v_mfma_scale_f32_16x16x128_f8f6f4 v[62:65], v[2:9], v[228:235], v[62:65], v200, v201 op_sel_hi:[0,0,0]
	v_mfma_scale_f32_16x16x128_f8f6f4 v[58:61], v[10:17], v[228:235], v[58:61], v200, v201 op_sel_hi:[0,0,0]
	v_mfma_scale_f32_16x16x128_f8f6f4 v[46:49], v[2:9], v[236:243], v[46:49], v200, v201 op_sel_hi:[0,0,0]
	v_mfma_scale_f32_16x16x128_f8f6f4 v[42:45], v[10:17], v[236:243], v[42:45], v200, v201 op_sel_hi:[0,0,0]
	v_mfma_scale_f32_16x16x128_f8f6f4 v[86:89], v[18:25], v[212:219], v[86:89], v200, v201 op_sel_hi:[0,0,0]
	v_mfma_scale_f32_16x16x128_f8f6f4 v[82:85], v[26:33], v[212:219], v[82:85], v200, v201 op_sel_hi:[0,0,0]
	v_mfma_scale_f32_16x16x128_f8f6f4 v[70:73], v[18:25], v[220:227], v[70:73], v200, v201 op_sel_hi:[0,0,0]
	v_mfma_scale_f32_16x16x128_f8f6f4 v[66:69], v[26:33], v[220:227], v[66:69], v200, v201 op_sel_hi:[0,0,0]
	v_mfma_scale_f32_16x16x128_f8f6f4 v[54:57], v[18:25], v[228:235], v[54:57], v200, v201 op_sel_hi:[0,0,0]
	v_mfma_scale_f32_16x16x128_f8f6f4 v[50:53], v[26:33], v[228:235], v[50:53], v200, v201 op_sel_hi:[0,0,0]
	v_mfma_scale_f32_16x16x128_f8f6f4 v[38:41], v[18:25], v[236:243], v[38:41], v200, v201 op_sel_hi:[0,0,0]
	v_mfma_scale_f32_16x16x128_f8f6f4 v[34:37], v[26:33], v[236:243], v[34:37], v200, v201 op_sel_hi:[0,0,0]
	s_setprio 0
	s_barrier
	s_add_u32 s46, s46, 0x100
	s_addc_u32 s47, s47, 0
	s_add_u32 s80, s80, 0x100
	s_addc_u32 s81, s81, 0
	s_cmp_ge_i32 s82, s58
	s_cselect_b32 s99, 0, 1
	s_mov_b32 s48, s82
	s_cbranch_scc0 .LBB0_1625

; #define PG8_STAGE(bufoff, gbase, voff) do { _Pragma("unroll") for (int _i = 0; _i < 2; ++_i) \
;         __builtin_amdgcn_global_load_lds((const unsigned*)((const char*)(gbase) + (voff)[_i]), (PG8_LAS unsigned*)(lds + (bufoff) + ldsw + _i * 8192), 16, 0, 0); } while (0)
; #define PG8_LDA(dst, b, h) do { _Pragma("unroll") for (int m = 0; m < 4; ++m) { const bf16x8 f0_ = *(const PG8_LAS bf16x8*)(lds + PG8_SA(b, h) + aoff + m * 2048), f1_ = *(const PG8_LAS bf16x8*)(lds + PG8_SA(b, h) + aoff + m * 2048 + 1024); dst[m].set(f0_, f1_); } } while (0)
; #define PG8_LDB(dst, b, h) do { _Pragma("unroll") for (int n = 0; n < 2; ++n) { const bf16x8 f0_ = *(const PG8_LAS bf16x8*)(lds + PG8_SB(b, h) + boff + n * 2048), f1_ = *(const PG8_LAS bf16x8*)(lds + PG8_SB(b, h) + boff + n * 2048 + 1024); dst[n].set(f0_, f1_); } } while (0)
; #define PG8_WAIT_V(n) asm volatile("s_waitcnt vmcnt(" #n ")" ::: "memory")
; #define PG8_WAIT_L(n) asm volatile("s_waitcnt lgkmcnt(" #n ")" ::: "memory")
; #define PG8_BAR __builtin_amdgcn_s_barrier()
; #define PG8_SCHED __builtin_amdgcn_sched_barrier(0)
; template <class Epi, class Sched, bool ALIGN_EPI = false, bool SP2 = false>
; __device__ __forceinline__ void gemm_phase(PG8_LAS unsigned char* lds, const Gemm g, const Sched& S, const Epi& E) {
;     ...
;             PG8_LDB(B0, 0, 0); PG8_LDB(B1, 0, 1); PG8_SCHED; PG8_LDA(At, 0, 0); PG8_STAGE(PG8_SA(1, 1), a1 + hstep, voffA);
;             PG8_WAIT_V(8); PG8_WAIT_L(0); PG8_BAR; PG8_MMA(0, 0, At, B0); PG8_MMA(0, 1, At, B1); PG8_BAR; PG8_SCHED;
;             PG8_LDA(At, 0, 1); PG8_STAGE(PG8_SB(0, 0), b2, voffB); PG8_STAGE(PG8_SB(0, 1), b2 + hstepB, voffB); PG8_STAGE(PG8_SA(0, 0), a2, voffA);
;             PG8_WAIT_V(8); PG8_WAIT_L(0); PG8_BAR; PG8_MMA(1, 0, At, B0); PG8_MMA(1, 1, At, B1); PG8_BAR; PG8_SCHED;
.Lkr6_a:
	v_lshl_add_u64 v[206:207], s[2:3], 0, v[198:199]
	s_add_i32 m0, s71, 0xc000
	ds_read_b128 v[152:155], v217
	ds_read_b128 v[156:159], v217 offset:1024
	ds_read_b128 v[168:171], v217 offset:2048
	ds_read_b128 v[172:175], v217 offset:3072
	ds_read_b128 v[176:179], v217 offset:4096
	ds_read_b128 v[180:183], v217 offset:5120
	ds_read_b128 v[226:229], v217 offset:6144
	ds_read_b128 v[230:233], v217 offset:7168
	global_load_lds_dwordx4 v[206:207], off
	v_lshl_add_u64 v[206:207], s[2:3], 0, v[200:201]
	s_add_i32 m0, s71, 0xe000
	s_nop 0
	global_load_lds_dwordx4 v[206:207], off
	s_waitcnt vmcnt(8)
	s_waitcnt lgkmcnt(0)
	s_setprio 1
	s_barrier
	v_mfma_scale_f32_16x16x128_f8f6f4 v[164:167], v[16:23], v[152:159], v[164:167], v218, v219 op_sel_hi:[0,0,0]
	v_mfma_scale_f32_16x16x128_f8f6f4 v[160:163], v[24:31], v[152:159], v[160:163], v218, v219 op_sel_hi:[0,0,0]
	v_mfma_scale_f32_16x16x128_f8f6f4 v[140:143], v[16:23], v[168:175], v[140:143], v218, v219 op_sel_hi:[0,0,0]
	v_mfma_scale_f32_16x16x128_f8f6f4 v[136:139], v[24:31], v[168:175], v[136:139], v218, v219 op_sel_hi:[0,0,0]
	v_mfma_scale_f32_16x16x128_f8f6f4 v[108:111], v[16:23], v[176:183], v[108:111], v218, v219 op_sel_hi:[0,0,0]
	v_mfma_scale_f32_16x16x128_f8f6f4 v[104:107], v[24:31], v[176:183], v[104:107], v218, v219 op_sel_hi:[0,0,0]
	v_mfma_scale_f32_16x16x128_f8f6f4 v[116:119], v[16:23], v[226:233], v[116:119], v218, v219 op_sel_hi:[0,0,0]
	v_mfma_scale_f32_16x16x128_f8f6f4 v[112:115], v[24:31], v[226:233], v[112:115], v218, v219 op_sel_hi:[0,0,0]
	v_mfma_scale_f32_16x16x128_f8f6f4 v[148:151], v[0:7], v[152:159], v[148:151], v218, v219 op_sel_hi:[0,0,0]
	v_mfma_scale_f32_16x16x128_f8f6f4 v[144:147], v[8:15], v[152:159], v[144:147], v218, v219 op_sel_hi:[0,0,0]
	v_mfma_scale_f32_16x16x128_f8f6f4 v[132:135], v[0:7], v[168:175], v[132:135], v218, v219 op_sel_hi:[0,0,0]
	v_mfma_scale_f32_16x16x128_f8f6f4 v[128:131], v[8:15], v[168:175], v[128:131], v218, v219 op_sel_hi:[0,0,0]
	v_mfma_scale_f32_16x16x128_f8f6f4 v[124:127], v[0:7], v[176:183], v[124:127], v218, v219 op_sel_hi:[0,0,0]
	v_mfma_scale_f32_16x16x128_f8f6f4 v[120:123], v[8:15], v[176:183], v[120:123], v218, v219 op_sel_hi:[0,0,0]
	v_mfma_scale_f32_16x16x128_f8f6f4 v[100:103], v[0:7], v[226:233], v[100:103], v218, v219 op_sel_hi:[0,0,0]
	v_mfma_scale_f32_16x16x128_f8f6f4 v[96:99], v[8:15], v[226:233], v[96:99], v218, v219 op_sel_hi:[0,0,0]
	s_setprio 0
	s_barrier
	s_add_i32 s0, s67, s45
	v_lshl_add_u64 v[152:153], s[80:81], 0, v[186:187]
	s_mov_b32 m0, s0
	ds_read_b128 v[172:175], v217 offset:16384
	ds_read_b128 v[176:179], v217 offset:17408
	ds_read_b128 v[226:229], v217 offset:18432
	ds_read_b128 v[230:233], v217 offset:19456
	ds_read_b128 v[234:237], v217 offset:20480
	ds_read_b128 v[238:241], v217 offset:21504
	ds_read_b128 v[242:245], v217 offset:22528
	ds_read_b128 v[246:249], v217 offset:23552
	global_load_lds_dwordx4 v[152:153], off
	s_add_i32 m0, s0, 0x2000
	s_add_u32 s0, s80, s20
	v_lshl_add_u64 v[154:155], s[80:81], 0, v[190:191]
	s_addc_u32 s1, s81, s21
	s_add_i32 s33, s10, s45
	global_load_lds_dwordx4 v[154:155], off
	v_lshl_add_u64 v[156:157], s[0:1], 0, v[186:187]
	s_mov_b32 m0, s33
	v_lshl_add_u64 v[158:159], s[0:1], 0, v[190:191]
	global_load_lds_dwordx4 v[156:157], off
	s_add_i32 m0, s33, 0x2000
	v_lshl_add_u64 v[168:169], s[78:79], 0, v[184:185]
	global_load_lds_dwordx4 v[158:159], off
	v_lshl_add_u64 v[170:171], s[78:79], 0, v[188:189]
	s_waitcnt vmcnt(6)
	s_waitcnt lgkmcnt(0)
	s_setprio 1
	s_barrier
	v_mfma_scale_f32_16x16x128_f8f6f4 v[92:95], v[16:23], v[172:179], v[92:95], v218, v219 op_sel_hi:[0,0,0]
	v_mfma_scale_f32_16x16x128_f8f6f4 v[88:91], v[24:31], v[172:179], v[88:91], v218, v219 op_sel_hi:[0,0,0]
	v_mfma_scale_f32_16x16x128_f8f6f4 v[76:79], v[16:23], v[226:233], v[76:79], v218, v219 op_sel_hi:[0,0,0]
	v_mfma_scale_f32_16x16x128_f8f6f4 v[72:75], v[24:31], v[226:233], v[72:75], v218, v219 op_sel_hi:[0,0,0]
	v_mfma_scale_f32_16x16x128_f8f6f4 v[60:63], v[16:23], v[234:241], v[60:63], v218, v219 op_sel_hi:[0,0,0]
	v_mfma_scale_f32_16x16x128_f8f6f4 v[56:59], v[24:31], v[234:241], v[56:59], v218, v219 op_sel_hi:[0,0,0]
	v_mfma_scale_f32_16x16x128_f8f6f4 v[44:47], v[16:23], v[242:249], v[44:47], v218, v219 op_sel_hi:[0,0,0]
	v_mfma_scale_f32_16x16x128_f8f6f4 v[40:43], v[24:31], v[242:249], v[40:43], v218, v219 op_sel_hi:[0,0,0]
	v_mfma_scale_f32_16x16x128_f8f6f4 v[84:87], v[0:7], v[172:179], v[84:87], v218, v219 op_sel_hi:[0,0,0]
	v_mfma_scale_f32_16x16x128_f8f6f4 v[80:83], v[8:15], v[172:179], v[80:83], v218, v219 op_sel_hi:[0,0,0]
	v_mfma_scale_f32_16x16x128_f8f6f4 v[68:71], v[0:7], v[226:233], v[68:71], v218, v219 op_sel_hi:[0,0,0]
	v_mfma_scale_f32_16x16x128_f8f6f4 v[64:67], v[8:15], v[226:233], v[64:67], v218, v219 op_sel_hi:[0,0,0]
	v_mfma_scale_f32_16x16x128_f8f6f4 v[52:55], v[0:7], v[234:241], v[52:55], v218, v219 op_sel_hi:[0,0,0]
	v_mfma_scale_f32_16x16x128_f8f6f4 v[48:51], v[8:15], v[234:241], v[48:51], v218, v219 op_sel_hi:[0,0,0]
	v_mfma_scale_f32_16x16x128_f8f6f4 v[36:39], v[0:7], v[242:249], v[36:39], v218, v219 op_sel_hi:[0,0,0]
	v_mfma_scale_f32_16x16x128_f8f6f4 v[32:35], v[8:15], v[242:249], v[32:35], v218, v219 op_sel_hi:[0,0,0]
	s_setprio 0
	s_barrier
; #define PG8_STAGE(bufoff, gbase, voff) do { _Pragma("unroll") for (int _i = 0; _i < 2; ++_i) \
;         __builtin_amdgcn_global_load_lds((const unsigned*)((const char*)(gbase) + (voff)[_i]), (PG8_LAS unsigned*)(lds + (bufoff) + ldsw + _i * 8192), 16, 0, 0); } while (0)
; #define PG8_LDA(dst, b, h) do { _Pragma("unroll") for (int m = 0; m < 4; ++m) { const bf16x8 f0_ = *(const PG8_LAS bf16x8*)(lds + PG8_SA(b, h) + aoff + m * 2048), f1_ = *(const PG8_LAS bf16x8*)(lds + PG8_SA(b, h) + aoff + m * 2048 + 1024); dst[m].set(f0_, f1_); } } while (0)
; #define PG8_LDB(dst, b, h) do { _Pragma("unroll") for (int n = 0; n < 2; ++n) { const bf16x8 f0_ = *(const PG8_LAS bf16x8*)(lds + PG8_SB(b, h) + boff + n * 2048), f1_ = *(const PG8_LAS bf16x8*)(lds + PG8_SB(b, h) + boff + n * 2048 + 1024); dst[n].set(f0_, f1_); } } while (0)
; #define PG8_WAIT_V(n) asm volatile("s_waitcnt vmcnt(" #n ")" ::: "memory")
; #define PG8_WAIT_L(n) asm volatile("s_waitcnt lgkmcnt(" #n ")" ::: "memory")
; #define PG8_BAR __builtin_amdgcn_s_barrier()
; #define PG8_SCHED __builtin_amdgcn_sched_barrier(0)
; template <class Epi, class Sched, bool ALIGN_EPI = false, bool SP2 = false>
; __device__ __forceinline__ void gemm_phase(PG8_LAS unsigned char* lds, const Gemm g, const Sched& S, const Epi& E) {
;     ...
;             PG8_LDB(B0, 1, 0); PG8_LDB(B1, 1, 1); PG8_SCHED; PG8_LDA(At, 1, 0); PG8_STAGE(PG8_SA(0, 1), a2 + hstep, voffA);
;             PG8_WAIT_V(8); PG8_WAIT_L(0); PG8_BAR; PG8_MMA(0, 0, At, B0); PG8_MMA(0, 1, At, B1); PG8_BAR; PG8_SCHED;
;             PG8_LDA(At, 1, 1); PG8_STAGE(PG8_SB(1, 0), b3, voffB); PG8_STAGE(PG8_SB(1, 1), b3 + hstepB, voffB); PG8_STAGE(PG8_SA(1, 0), a3, voffA);
;             PG8_WAIT_V(8); PG8_WAIT_L(0); PG8_BAR; PG8_MMA(1, 0, At, B0); PG8_MMA(1, 1, At, B1); PG8_BAR; PG8_SCHED;
	s_add_i32 s33, 0, 0x18000
	s_add_i32 s80, 0, 0x1c000
	v_add_u32_e32 v12, s33, v211
	v_add_u32_e32 v28, s80, v211
	ds_read_b128 v[0:3], v12
	ds_read_b128 v[4:7], v12 offset:1024
	ds_read_b128 v[8:11], v12 offset:2048
	ds_read_b128 v[12:15], v12 offset:3072
	ds_read_b128 v[16:19], v28
	ds_read_b128 v[20:23], v28 offset:1024
	ds_read_b128 v[24:27], v28 offset:2048
	ds_read_b128 v[28:31], v28 offset:3072
	s_add_u32 s0, s78, s18
	s_addc_u32 s1, s79, s19
	s_mov_b32 m0, s86
	v_lshl_add_u64 v[180:181], s[0:1], 0, v[184:185]
	ds_read_b128 v[172:175], v217 offset:32768
	ds_read_b128 v[176:179], v217 offset:33792
	ds_read_b128 v[226:229], v217 offset:34816
	ds_read_b128 v[230:233], v217 offset:35840
	ds_read_b128 v[234:237], v217 offset:36864
	ds_read_b128 v[238:241], v217 offset:37888
	ds_read_b128 v[242:245], v217 offset:38912
	ds_read_b128 v[246:249], v217 offset:39936
	s_mov_b32 m0, s71
	s_nop 0
	global_load_lds_dwordx4 v[168:169], off
	s_mov_b32 m0, s73
	s_nop 0
	global_load_lds_dwordx4 v[170:171], off
	s_mov_b32 m0, s86
	s_nop 0
	global_load_lds_dwordx4 v[180:181], off
	v_lshl_add_u64 v[180:181], s[0:1], 0, v[188:189]
	s_mov_b32 m0, s87
	s_nop 0
	global_load_lds_dwordx4 v[180:181], off
	s_waitcnt vmcnt(8)
	s_waitcnt lgkmcnt(0)
	s_setprio 1
	s_barrier
	v_mfma_scale_f32_16x16x128_f8f6f4 v[164:167], v[0:7], v[172:179], v[164:167], v218, v219 op_sel_hi:[0,0,0]
	v_mfma_scale_f32_16x16x128_f8f6f4 v[160:163], v[8:15], v[172:179], v[160:163], v218, v219 op_sel_hi:[0,0,0]
	v_mfma_scale_f32_16x16x128_f8f6f4 v[140:143], v[0:7], v[226:233], v[140:143], v218, v219 op_sel_hi:[0,0,0]
	v_mfma_scale_f32_16x16x128_f8f6f4 v[136:139], v[8:15], v[226:233], v[136:139], v218, v219 op_sel_hi:[0,0,0]
	v_mfma_scale_f32_16x16x128_f8f6f4 v[108:111], v[0:7], v[234:241], v[108:111], v218, v219 op_sel_hi:[0,0,0]
	v_mfma_scale_f32_16x16x128_f8f6f4 v[104:107], v[8:15], v[234:241], v[104:107], v218, v219 op_sel_hi:[0,0,0]
	v_mfma_scale_f32_16x16x128_f8f6f4 v[116:119], v[0:7], v[242:249], v[116:119], v218, v219 op_sel_hi:[0,0,0]
	v_mfma_scale_f32_16x16x128_f8f6f4 v[112:115], v[8:15], v[242:249], v[112:115], v218, v219 op_sel_hi:[0,0,0]
	v_mfma_scale_f32_16x16x128_f8f6f4 v[148:151], v[16:23], v[172:179], v[148:151], v218, v219 op_sel_hi:[0,0,0]
	v_mfma_scale_f32_16x16x128_f8f6f4 v[144:147], v[24:31], v[172:179], v[144:147], v218, v219 op_sel_hi:[0,0,0]
	v_mfma_scale_f32_16x16x128_f8f6f4 v[132:135], v[16:23], v[226:233], v[132:135], v218, v219 op_sel_hi:[0,0,0]
	v_mfma_scale_f32_16x16x128_f8f6f4 v[128:131], v[24:31], v[226:233], v[128:131], v218, v219 op_sel_hi:[0,0,0]
	v_mfma_scale_f32_16x16x128_f8f6f4 v[124:127], v[16:23], v[234:241], v[124:127], v218, v219 op_sel_hi:[0,0,0]
	v_mfma_scale_f32_16x16x128_f8f6f4 v[120:123], v[24:31], v[234:241], v[120:123], v218, v219 op_sel_hi:[0,0,0]
	v_mfma_scale_f32_16x16x128_f8f6f4 v[100:103], v[16:23], v[242:249], v[100:103], v218, v219 op_sel_hi:[0,0,0]
	v_mfma_scale_f32_16x16x128_f8f6f4 v[96:99], v[24:31], v[242:249], v[96:99], v218, v219 op_sel_hi:[0,0,0]
	s_setprio 0
	s_barrier
	s_add_i32 s0, s33, s45
	v_lshl_add_u64 v[152:153], v[152:153], 0, s[36:37]
	s_mov_b32 m0, s0
	ds_read_b128 v[172:175], v217 offset:49152
	ds_read_b128 v[176:179], v217 offset:50176
	ds_read_b128 v[226:229], v217 offset:51200
	ds_read_b128 v[230:233], v217 offset:52224
	ds_read_b128 v[234:237], v217 offset:53248
	ds_read_b128 v[238:241], v217 offset:54272
	ds_read_b128 v[242:245], v217 offset:55296
	ds_read_b128 v[246:249], v217 offset:56320
	global_load_lds_dwordx4 v[152:153], off
	v_lshl_add_u64 v[152:153], v[154:155], 0, s[36:37]
	s_add_i32 m0, s0, 0x2000
	s_add_i32 s0, s80, s45
	global_load_lds_dwordx4 v[152:153], off
	v_lshl_add_u64 v[152:153], v[156:157], 0, s[36:37]
	s_mov_b32 m0, s0
	s_nop 0
	global_load_lds_dwordx4 v[152:153], off
	v_lshl_add_u64 v[152:153], v[158:159], 0, s[36:37]
	s_add_i32 m0, s0, 0x2000
	s_nop 0
	global_load_lds_dwordx4 v[152:153], off
	s_cmp_ge_i32 s83, s91
	s_cbranch_scc0 .Lkr6_b
	v_lshl_add_u64 v[152:153], v[168:169], 0, s[36:37]
	s_mov_b32 m0, s93
	s_nop 0
	global_load_lds_dwordx4 v[152:153], off
	v_lshl_add_u64 v[152:153], v[170:171], 0, s[36:37]
	s_mov_b32 m0, s94
	s_nop 0
	global_load_lds_dwordx4 v[152:153], off
.Lkr6_b:
	s_waitcnt vmcnt(6)
	s_waitcnt lgkmcnt(0)
	s_setprio 1
	s_barrier
	v_mfma_scale_f32_16x16x128_f8f6f4 v[92:95], v[0:7], v[172:179], v[92:95], v218, v219 op_sel_hi:[0,0,0]
	v_mfma_scale_f32_16x16x128_f8f6f4 v[88:91], v[8:15], v[172:179], v[88:91], v218, v219 op_sel_hi:[0,0,0]
	v_mfma_scale_f32_16x16x128_f8f6f4 v[76:79], v[0:7], v[226:233], v[76:79], v218, v219 op_sel_hi:[0,0,0]
	v_mfma_scale_f32_16x16x128_f8f6f4 v[72:75], v[8:15], v[226:233], v[72:75], v218, v219 op_sel_hi:[0,0,0]
	v_mfma_scale_f32_16x16x128_f8f6f4 v[60:63], v[0:7], v[234:241], v[60:63], v218, v219 op_sel_hi:[0,0,0]
	v_mfma_scale_f32_16x16x128_f8f6f4 v[56:59], v[8:15], v[234:241], v[56:59], v218, v219 op_sel_hi:[0,0,0]
	v_mfma_scale_f32_16x16x128_f8f6f4 v[44:47], v[0:7], v[242:249], v[44:47], v218, v219 op_sel_hi:[0,0,0]
	v_mfma_scale_f32_16x16x128_f8f6f4 v[40:43], v[8:15], v[242:249], v[40:43], v218, v219 op_sel_hi:[0,0,0]
	v_mfma_scale_f32_16x16x128_f8f6f4 v[84:87], v[16:23], v[172:179], v[84:87], v218, v219 op_sel_hi:[0,0,0]
	v_mfma_scale_f32_16x16x128_f8f6f4 v[80:83], v[24:31], v[172:179], v[80:83], v218, v219 op_sel_hi:[0,0,0]
	v_mfma_scale_f32_16x16x128_f8f6f4 v[68:71], v[16:23], v[226:233], v[68:71], v218, v219 op_sel_hi:[0,0,0]
	v_mfma_scale_f32_16x16x128_f8f6f4 v[64:67], v[24:31], v[226:233], v[64:67], v218, v219 op_sel_hi:[0,0,0]
	v_mfma_scale_f32_16x16x128_f8f6f4 v[52:55], v[16:23], v[234:241], v[52:55], v218, v219 op_sel_hi:[0,0,0]
	v_mfma_scale_f32_16x16x128_f8f6f4 v[48:51], v[24:31], v[234:241], v[48:51], v218, v219 op_sel_hi:[0,0,0]
	v_mfma_scale_f32_16x16x128_f8f6f4 v[36:39], v[16:23], v[242:249], v[36:39], v218, v219 op_sel_hi:[0,0,0]
	v_mfma_scale_f32_16x16x128_f8f6f4 v[32:35], v[24:31], v[242:249], v[32:35], v218, v219 op_sel_hi:[0,0,0]
	s_setprio 0
	s_barrier
	s_add_u32 s2, s2, 0x100
	s_addc_u32 s3, s3, 0
	s_add_u32 s57, s57, 0x100
	s_addc_u32 s82, s82, 0
	s_cmp_ge_i32 s83, s91
	s_cselect_b32 s99, 0, 1
	s_mov_b32 s78, s83
	s_cbranch_scc0 .LBB0_1658
